# speedup vs baseline: 1.0058x; 1.0030x over previous
_Z6k_gemmI4Epi8ILi0ELb1ELb1EEEv4GemmT_iiii:
	s_load_dwordx4 s[4:7], s[0:1], 0x38
	s_waitcnt lgkmcnt(0)
	s_mul_i32 s3, s5, s4
	s_mul_i32 s20, s3, s6
	s_cmp_ge_i32 s2, s20
	v_readfirstlane_b32 s3, v0
	s_cbranch_scc1 .LBB4_20
	s_ashr_i32 s21, s20, 31
	s_load_dword s34, s[0:1], 0x10
	s_load_dwordx4 s[16:19], s[0:1], 0x0
	s_load_dwordx8 s[8:15], s[0:1], 0x18
	s_load_dword s33, s[0:1], 0x48
	s_lshr_b32 s0, s21, 29
	v_lshrrev_b32_e32 v5, 5, v0
	s_add_i32 s0, s20, s0
	v_lshlrev_b32_e32 v3, 4, v0
	v_and_b32_e32 v5, 4, v5
	v_lshrrev_b32_e32 v6, 3, v0
	v_lshrrev_b32_e32 v7, 2, v0
	v_lshrrev_b32_e32 v18, 1, v0
	v_lshlrev_b32_e32 v9, 1, v0
	s_ashr_i32 s0, s0, 3
	v_and_b32_e32 v2, 16, v0
	v_and_b32_e32 v4, 0x70, v3
	v_and_b32_e32 v7, 64, v7
	v_and_or_b32 v5, v6, 3, v5
	v_and_b32_e32 v8, 48, v18
	v_and_b32_e32 v9, 64, v9
	s_ff1_i32_b32 s50, s0
	s_lshl_b32 s0, s6, 3
	v_or3_b32 v7, v8, v7, v5
	v_bitop3_b32 v2, v9, v4, v2 bitop3:0x36
	s_ff1_i32_b32 s51, s0
	s_waitcnt lgkmcnt(0)
	v_mad_u64_u32 v[146:147], s[0:1], s34, v6, v[2:3]
	v_mad_u64_u32 v[148:149], s[0:1], s34, v7, v[2:3]
	v_or_b32_e32 v3, 0x2000, v3
	v_lshrrev_b32_e32 v4, 7, v3
	v_lshrrev_b32_e32 v3, 6, v3
	v_and_b32_e32 v3, 0xc0, v3
	v_or3_b32 v3, v8, v3, v5
	s_lshr_b32 s28, s3, 6
	v_mad_u64_u32 v[150:151], s[0:1], s34, v4, v[2:3]
	v_mad_u64_u32 v[152:153], s[0:1], s34, v3, v[2:3]
	s_lshl_b32 s0, s28, 10
	s_add_i32 s54, s0, 0
	s_and_b32 s0, s2, 7
	s_lshl_b32 s0, s0, s50
	s_ashr_i32 s1, s2, 3
	s_add_i32 s0, s0, s1
	s_lshl_b32 s30, -1, s51
	s_ashr_i32 s1, s0, s51
	s_andn2_b32 s0, s0, s30
	s_lshl_b32 s1, s1, 3
	s_and_b32 s28, s0, 7
	s_ashr_i32 s35, s34, 31
	s_ff1_i32_b32 s52, s5
	s_or_b32 s77, s1, s28
	s_bfe_u32 s4, s3, 0x20006
	s_lshr_b32 s15, s3, 8
	s_lshl_b64 s[22:23], s[34:35], 7
	s_lshl_b64 s[24:25], s[34:35], 3
	s_lshl_b64 s[26:27], s[34:35], 8
	s_lshr_b32 s76, s0, 3
	s_ashr_i32 s0, s77, s52
	s_add_i32 s1, s5, -1
	s_cmp_lg_u32 s7, 0
	s_cselect_b32 s7, s1, -1
	s_and_b32 s5, s77, s7
	s_mul_i32 s0, s0, s6
	s_add_i32 s28, s0, s76
	s_ashr_i32 s0, s5, 31
	s_mul_i32 s0, s26, s0
	s_mul_hi_u32 s1, s26, s5
	s_add_i32 s29, s1, s0
	s_lshr_b64 s[0:1], s[34:35], 24
	s_mul_i32 s1, s0, s5
	s_add_i32 s31, s29, s1
	s_ashr_i32 s29, s28, 31
	s_mul_i32 s36, s26, s5
	s_mul_i32 s1, s26, s29
	s_mul_hi_u32 s5, s26, s28
	s_add_i32 s1, s5, s1
	s_mul_i32 s0, s0, s28
	s_add_i32 s1, s1, s0
	s_mul_i32 s0, s26, s28
	s_add_u32 s38, s18, s0
	v_bfe_u32 v1, v0, 4, 2
	s_addc_u32 s39, s19, s1
	s_lshl_b64 s[0:1], s[28:29], 10
	v_lshlrev_b32_e32 v2, 6, v1
	s_add_u32 s0, s10, s0
	v_lshl_or_b32 v147, s4, 8, v2
	s_addc_u32 s1, s11, s1
	global_load_dwordx4 v[14:17], v147, s[0:1]
	global_load_dwordx4 v[10:13], v147, s[0:1] offset:16
	global_load_dwordx4 v[6:9], v147, s[0:1] offset:32
	global_load_dwordx4 v[2:5], v147, s[0:1] offset:48
	s_add_i32 s55, s54, 0x10000
	s_mov_b32 m0, s55
	s_nop 0
	global_load_lds_dwordx4 v148, s[38:39] sc1
	s_add_i32 s56, s54, 0x12000
	s_mov_b32 m0, s56
	s_nop 0
	global_load_lds_dwordx4 v152, s[38:39] sc1
	s_add_u32 s40, s16, s36
	s_addc_u32 s41, s17, s31
	s_mov_b32 m0, s54
	s_nop 0
	global_load_lds_dwordx4 v146, s[40:41] sc1
	s_add_i32 s57, s54, 0x2000
	s_add_i32 s58, s54, 0x14000
	s_mov_b32 m0, s57
	s_nop 0
	global_load_lds_dwordx4 v150, s[40:41] sc1
	s_add_u32 s0, s38, s24
	s_addc_u32 s1, s39, s25
	s_mov_b32 m0, s58
	s_nop 0
	global_load_lds_dwordx4 v148, s[0:1] sc1
	s_add_i32 s59, s54, 0x16000
	s_add_i32 s60, s54, 0x4000
	s_mov_b32 m0, s59
	s_nop 0
	global_load_lds_dwordx4 v152, s[0:1] sc1
	s_add_u32 s36, s40, s22
	s_addc_u32 s37, s41, s23
	s_mov_b32 m0, s60
	s_nop 0
	global_load_lds_dwordx4 v146, s[36:37] sc1
	s_add_i32 s61, s54, 0x6000
	s_mov_b32 m0, s61
	s_nop 0
	global_load_lds_dwordx4 v150, s[36:37] sc1
	s_mov_b32 s53, 0
	s_mov_b32 s5, 0x10000
	s_cmp_lg_u32 s15, 1
	s_cbranch_scc1 .LBB4_3
.LBB4_3:
	s_lshr_b32 s29, s35, 25
	s_add_i32 s29, s34, s29
	s_not_b32 s62, s30
	s_ashr_i32 s63, s29, 7
	s_add_i32 s64, s54, 0x18000
	v_and_b32_e32 v19, 15, v0
	v_and_b32_e32 v0, 4, v0
	s_add_u32 s30, s38, 0x80
	v_lshl_or_b32 v149, s15, 6, v19
	v_lshlrev_b32_e32 v20, 5, v1
	v_and_or_b32 v0, v18, 1, v0
	s_waitcnt vmcnt(0)
	s_barrier
	s_addc_u32 s31, s39, 0
	s_mov_b32 m0, s64
	s_nop 0
	global_load_lds_dwordx4 v148, s[30:31] sc1
	s_add_i32 s65, s54, 0x1a000
	s_add_i32 s66, s54, 0x8000
	v_lshlrev_b32_e32 v21, 7, v149
	v_lshlrev_b32_e32 v0, 4, v0
	v_or_b32_e32 v23, 16, v20
	s_mov_b32 m0, s65
	s_nop 0
	global_load_lds_dwordx4 v152, s[30:31] sc1
	s_add_u32 s30, s40, 0x80
	v_xor_b32_e32 v18, v0, v20
	v_bitop3_b32 v22, v21, v0, v20 bitop3:0xf6
	v_bitop3_b32 v20, v0, v20, 16 bitop3:0x1e
	v_bitop3_b32 v21, v21, v0, v23 bitop3:0xf6
	v_lshlrev_b32_e32 v0, 7, v19
	s_addc_u32 s31, s41, 0
	s_mov_b32 m0, s66
	s_nop 0
	global_load_lds_dwordx4 v146, s[30:31] sc1
	s_add_i32 s67, s54, 0xa000
	s_add_i32 s68, s54, 0x1c000
	v_lshl_or_b32 v0, s4, 12, v0
	s_mov_b32 m0, s67
	s_nop 0
	global_load_lds_dwordx4 v150, s[30:31] sc1
	s_add_u32 s0, s0, 0x80
	v_or3_b32 v18, v18, v0, s5
	v_or3_b32 v19, v20, v0, s5
	s_addc_u32 s1, s1, 0
	s_mov_b32 m0, s68
	s_nop 0
	global_load_lds_dwordx4 v148, s[0:1] sc1
	v_lshlrev_b32_e32 v0, 4, v1
	s_add_i32 s69, s54, 0x1e000
	s_mov_b32 m0, s69
	s_nop 0
	global_load_lds_dwordx4 v152, s[0:1] sc1
	v_and_b32_e32 v1, 32, v0
	v_and_b32_e32 v153, 16, v0
	v_or_b32_e32 v158, 32, v0
	v_div_scale_f32 v0, s[0:1], s13, s13, 1.0
	v_lshl_or_b32 v151, s4, 6, v1
	v_rcp_f32_e32 v1, v0
	s_cmpk_gt_i32 s34, 0x7f
	s_cselect_b64 s[30:31], -1, 0
	s_add_i32 s70, s54, 0xc000
	v_fma_f32 v20, -v0, v1, 1.0
	v_fmac_f32_e32 v1, v20, v1
	v_div_scale_f32 v20, vcc, 1.0, s13, 1.0
	v_mul_f32_e32 v23, v20, v1
	v_fma_f32 v24, -v0, v23, v20
	v_fmac_f32_e32 v23, v24, v1
	v_fma_f32 v0, -v0, v23, v20
	v_div_fmas_f32 v0, v0, v1, v23
	v_mov_b32_e32 v1, s14
	v_mul_f32_e32 v1, s13, v1
	v_div_scale_f32 v20, s[0:1], v1, v1, 1.0
	v_rcp_f32_e32 v23, v20
	s_add_i32 s71, s54, 0xe000
	s_ashr_i32 s72, s33, 31
	s_ashr_i32 s73, s2, 31
	v_fma_f32 v24, -v20, v23, 1.0
	v_fmac_f32_e32 v23, v24, v23
	v_div_scale_f32 v24, vcc, 1.0, v1, 1.0
	v_mul_f32_e32 v25, v24, v23
	v_fma_f32 v26, -v20, v25, v24
	v_fmac_f32_e32 v25, v26, v23
	v_fma_f32 v20, -v20, v25, v24
	s_waitcnt vmcnt(6)
	v_div_fmas_f32 v20, v20, v23, v25
	s_cmp_eq_u32 s63, 2
	v_div_fixup_f32 v0, v0, s13, 1.0
	v_div_fixup_f32 v159, v20, v1, 1.0
	s_cselect_b64 s[14:15], -1, 0
	s_cmpk_gt_u32 s34, 0x17f
	v_mov_b32_e32 v154, v0
	v_mov_b32_e32 v155, v0
	v_mul_f32_e32 v160, 0x40c00000, v159
	s_cselect_b64 s[34:35], -1, 0
	v_add_u32_e32 v161, 0, v18
	v_add_u32_e32 v162, 0, v19
	v_add_u32_e32 v163, 0, v22
	v_add_u32_e32 v164, 0, v21
	s_barrier
	s_branch .LBB4_5

.Lrs_a_4:
	s_add_u32 s81, s40, s22
	s_addc_u32 s82, s41, s23
	s_add_u32 s29, s40, 0x100
	s_addc_u32 s44, s41, 0
	s_and_b64 s[42:43], s[14:15], exec
	ds_read_b128 v[82:85], v161
	ds_read_b128 v[94:97], v161 offset:2048
	ds_read_b128 v[102:105], v162
	ds_read_b128 v[110:113], v162 offset:2048
	s_cselect_b32 s47, s37, s44
	s_cselect_b32 s46, s36, s29
	s_add_u32 s29, s38, 0x100
	s_addc_u32 s44, s39, 0
	s_and_b64 s[42:43], s[14:15], exec
	s_cselect_b32 s49, s5, s44
	s_cselect_b32 s48, s4, s29
	s_add_u32 s44, s46, 0x80
	s_addc_u32 s45, s47, 0
	s_add_u32 s42, s48, 0x80
	s_addc_u32 s43, s49, 0
	ds_read_b128 v[58:61], v163
	ds_read_b128 v[66:69], v163 offset:2048
	ds_read_b128 v[62:65], v164
	ds_read_b128 v[70:73], v164 offset:2048
	ds_read_b128 v[74:77], v163 offset:4096
	ds_read_b128 v[86:89], v163 offset:6144
	ds_read_b128 v[78:81], v164 offset:4096
	ds_read_b128 v[90:93], v164 offset:6144
	s_add_u32 s78, s81, 0x80
	s_addc_u32 s79, s82, 0
	s_mov_b32 m0, s70
	s_nop 0
	global_load_lds_dwordx4 v146, s[78:79] sc1
	s_mov_b32 m0, s71
	s_nop 0
	global_load_lds_dwordx4 v150, s[78:79] sc1
	s_waitcnt lgkmcnt(8)
	ds_read_b128 v[142:145], v161 offset:16384
	ds_read_b128 v[166:169], v161 offset:18432
	ds_read_b128 v[170:173], v162 offset:16384
	ds_read_b128 v[174:177], v162 offset:18432
	s_waitcnt vmcnt(8)
	s_waitcnt lgkmcnt(0)
	s_barrier
	s_waitcnt lgkmcnt(0)
	s_waitcnt vmcnt(16)
	v_mov_b32_e32 v1, v0
	v_pk_mul_f32 v[16:17], v[0:1], v[16:17]
	v_pk_mul_f32 v[14:15], v[154:155], v[14:15]
	v_pk_mul_f32 v[12:13], v[0:1], v[12:13]
	v_pk_mul_f32 v[10:11], v[154:155], v[10:11]
	v_pk_mul_f32 v[8:9], v[0:1], v[8:9]
	v_pk_mul_f32 v[6:7], v[154:155], v[6:7]
	v_pk_mul_f32 v[4:5], v[0:1], v[4:5]
	v_pk_mul_f32 v[2:3], v[154:155], v[2:3]
	s_setprio 1
	v_mfma_f32_16x16x128_f8f6f4 v[18:21], v[82:85], v[58:61], v[14:17] cbsz:4 blgp:4
	v_mfma_f32_16x16x128_f8f6f4 v[18:21], v[102:105], v[62:65], v[18:21] cbsz:4 blgp:4
	v_mfma_f32_16x16x128_f8f6f4 v[22:25], v[94:97], v[58:61], v[10:13] cbsz:4 blgp:4
	v_mfma_f32_16x16x128_f8f6f4 v[22:25], v[110:113], v[62:65], v[22:25] cbsz:4 blgp:4
	v_mfma_f32_16x16x128_f8f6f4 v[26:29], v[82:85], v[66:69], v[14:17] cbsz:4 blgp:4
	v_mfma_f32_16x16x128_f8f6f4 v[26:29], v[102:105], v[70:73], v[26:29] cbsz:4 blgp:4
	v_mfma_f32_16x16x128_f8f6f4 v[30:33], v[94:97], v[66:69], v[10:13] cbsz:4 blgp:4
	v_mfma_f32_16x16x128_f8f6f4 v[30:33], v[110:113], v[70:73], v[30:33] cbsz:4 blgp:4
	v_mfma_f32_16x16x128_f8f6f4 v[34:37], v[82:85], v[74:77], v[14:17] cbsz:4 blgp:4
	v_mfma_f32_16x16x128_f8f6f4 v[34:37], v[102:105], v[78:81], v[34:37] cbsz:4 blgp:4
	v_mfma_f32_16x16x128_f8f6f4 v[38:41], v[94:97], v[74:77], v[10:13] cbsz:4 blgp:4
	v_mfma_f32_16x16x128_f8f6f4 v[38:41], v[110:113], v[78:81], v[38:41] cbsz:4 blgp:4
	v_mfma_f32_16x16x128_f8f6f4 v[42:45], v[82:85], v[86:89], v[14:17] cbsz:4 blgp:4
	v_mfma_f32_16x16x128_f8f6f4 v[42:45], v[102:105], v[90:93], v[42:45] cbsz:4 blgp:4
	v_mfma_f32_16x16x128_f8f6f4 v[46:49], v[94:97], v[86:89], v[10:13] cbsz:4 blgp:4
	v_mfma_f32_16x16x128_f8f6f4 v[46:49], v[110:113], v[90:93], v[46:49] cbsz:4 blgp:4
	v_mfma_f32_16x16x128_f8f6f4 v[50:53], v[142:145], v[58:61], v[6:9] cbsz:4 blgp:4
	v_mfma_f32_16x16x128_f8f6f4 v[50:53], v[170:173], v[62:65], v[50:53] cbsz:4 blgp:4
	v_mfma_f32_16x16x128_f8f6f4 v[54:57], v[166:169], v[58:61], v[2:5] cbsz:4 blgp:4
	v_mfma_f32_16x16x128_f8f6f4 v[54:57], v[174:177], v[62:65], v[54:57] cbsz:4 blgp:4
	v_mfma_f32_16x16x128_f8f6f4 v[58:61], v[142:145], v[66:69], v[6:9] cbsz:4 blgp:4
	v_mfma_f32_16x16x128_f8f6f4 v[58:61], v[170:173], v[70:73], v[58:61] cbsz:4 blgp:4
	v_mfma_f32_16x16x128_f8f6f4 v[62:65], v[166:169], v[66:69], v[2:5] cbsz:4 blgp:4
	v_mfma_f32_16x16x128_f8f6f4 v[62:65], v[174:177], v[70:73], v[62:65] cbsz:4 blgp:4
	v_mfma_f32_16x16x128_f8f6f4 v[66:69], v[142:145], v[74:77], v[6:9] cbsz:4 blgp:4
	v_mfma_f32_16x16x128_f8f6f4 v[66:69], v[170:173], v[78:81], v[66:69] cbsz:4 blgp:4
	v_mfma_f32_16x16x128_f8f6f4 v[70:73], v[166:169], v[74:77], v[2:5] cbsz:4 blgp:4
	v_mfma_f32_16x16x128_f8f6f4 v[70:73], v[174:177], v[78:81], v[70:73] cbsz:4 blgp:4
	v_mfma_f32_16x16x128_f8f6f4 v[74:77], v[142:145], v[86:89], v[6:9] cbsz:4 blgp:4
	v_mfma_f32_16x16x128_f8f6f4 v[74:77], v[170:173], v[90:93], v[74:77] cbsz:4 blgp:4
	v_mfma_f32_16x16x128_f8f6f4 v[78:81], v[166:169], v[86:89], v[2:5] cbsz:4 blgp:4
	v_mfma_f32_16x16x128_f8f6f4 v[78:81], v[174:177], v[90:93], v[78:81] cbsz:4 blgp:4
	s_setprio 0
	s_barrier
	s_mov_b32 m0, s55
	s_nop 0
	global_load_lds_dwordx4 v148, s[48:49] sc1
	s_mov_b32 m0, s56
	s_nop 0
	global_load_lds_dwordx4 v152, s[48:49] sc1
	ds_read_b128 v[114:117], v163 offset:16384
	ds_read_b128 v[122:125], v163 offset:18432
	ds_read_b128 v[130:133], v164 offset:16384
	ds_read_b128 v[134:137], v164 offset:18432
	ds_read_b128 v[178:181], v163 offset:20480
	ds_read_b128 v[182:185], v163 offset:22528
	ds_read_b128 v[186:189], v164 offset:20480
	ds_read_b128 v[190:193], v164 offset:22528
	s_mov_b32 m0, s54
	s_nop 0
	global_load_lds_dwordx4 v146, s[46:47] sc1
	s_mov_b32 m0, s57
	s_nop 0
	global_load_lds_dwordx4 v150, s[46:47] sc1
	s_add_u32 s48, s48, s24
	s_addc_u32 s49, s49, s25
	s_mov_b32 m0, s58
	s_nop 0
	global_load_lds_dwordx4 v148, s[48:49] sc1
	s_mov_b32 m0, s59
	s_nop 0
	global_load_lds_dwordx4 v152, s[48:49] sc1
	s_waitcnt vmcnt(8)
	s_waitcnt lgkmcnt(0)
	s_barrier
	s_setprio 1
	v_mfma_f32_16x16x128_f8f6f4 v[86:89], v[82:85], v[114:117], v[14:17] cbsz:4 blgp:4
	v_mfma_f32_16x16x128_f8f6f4 v[86:89], v[102:105], v[130:133], v[86:89] cbsz:4 blgp:4
	v_mfma_f32_16x16x128_f8f6f4 v[90:93], v[94:97], v[114:117], v[10:13] cbsz:4 blgp:4
	v_mfma_f32_16x16x128_f8f6f4 v[90:93], v[110:113], v[130:133], v[90:93] cbsz:4 blgp:4
	v_mfma_f32_16x16x128_f8f6f4 v[98:101], v[82:85], v[122:125], v[14:17] cbsz:4 blgp:4
	v_mfma_f32_16x16x128_f8f6f4 v[98:101], v[102:105], v[134:137], v[98:101] cbsz:4 blgp:4
	v_mfma_f32_16x16x128_f8f6f4 v[106:109], v[94:97], v[122:125], v[10:13] cbsz:4 blgp:4
	v_mfma_f32_16x16x128_f8f6f4 v[106:109], v[110:113], v[134:137], v[106:109] cbsz:4 blgp:4
	v_mfma_f32_16x16x128_f8f6f4 v[118:121], v[82:85], v[178:181], v[14:17] cbsz:4 blgp:4
	v_mfma_f32_16x16x128_f8f6f4 v[118:121], v[102:105], v[186:189], v[118:121] cbsz:4 blgp:4
	v_mfma_f32_16x16x128_f8f6f4 v[126:129], v[94:97], v[178:181], v[10:13] cbsz:4 blgp:4
	v_mfma_f32_16x16x128_f8f6f4 v[126:129], v[110:113], v[186:189], v[126:129] cbsz:4 blgp:4
	v_mfma_f32_16x16x128_f8f6f4 v[138:141], v[82:85], v[182:185], v[14:17] cbsz:4 blgp:4
	v_mfma_f32_16x16x128_f8f6f4 v[138:141], v[102:105], v[190:193], v[138:141] cbsz:4 blgp:4
	v_mfma_f32_16x16x128_f8f6f4 v[82:85], v[94:97], v[182:185], v[10:13] cbsz:4 blgp:4
	v_mfma_f32_16x16x128_f8f6f4 v[82:85], v[110:113], v[190:193], v[82:85] cbsz:4 blgp:4
	v_mfma_f32_16x16x128_f8f6f4 v[94:97], v[142:145], v[114:117], v[6:9] cbsz:4 blgp:4
	v_mfma_f32_16x16x128_f8f6f4 v[94:97], v[170:173], v[130:133], v[94:97] cbsz:4 blgp:4
	v_mfma_f32_16x16x128_f8f6f4 v[102:105], v[166:169], v[114:117], v[2:5] cbsz:4 blgp:4
	v_mfma_f32_16x16x128_f8f6f4 v[102:105], v[174:177], v[130:133], v[102:105] cbsz:4 blgp:4
	v_mfma_f32_16x16x128_f8f6f4 v[110:113], v[142:145], v[122:125], v[6:9] cbsz:4 blgp:4
	v_mfma_f32_16x16x128_f8f6f4 v[110:113], v[170:173], v[134:137], v[110:113] cbsz:4 blgp:4
	v_mfma_f32_16x16x128_f8f6f4 v[114:117], v[166:169], v[122:125], v[2:5] cbsz:4 blgp:4
	v_mfma_f32_16x16x128_f8f6f4 v[114:117], v[174:177], v[134:137], v[114:117] cbsz:4 blgp:4
	v_mfma_f32_16x16x128_f8f6f4 v[122:125], v[142:145], v[178:181], v[6:9] cbsz:4 blgp:4
	v_mfma_f32_16x16x128_f8f6f4 v[122:125], v[170:173], v[186:189], v[122:125] cbsz:4 blgp:4
	v_mfma_f32_16x16x128_f8f6f4 v[130:133], v[166:169], v[178:181], v[2:5] cbsz:4 blgp:4
	v_mfma_f32_16x16x128_f8f6f4 v[130:133], v[174:177], v[186:189], v[130:133] cbsz:4 blgp:4
	v_mfma_f32_16x16x128_f8f6f4 v[134:137], v[142:145], v[182:185], v[6:9] cbsz:4 blgp:4
	v_mfma_f32_16x16x128_f8f6f4 v[134:137], v[170:173], v[190:193], v[134:137] cbsz:4 blgp:4
	v_mfma_f32_16x16x128_f8f6f4 v[142:145], v[166:169], v[182:185], v[2:5] cbsz:4 blgp:4
	v_mfma_f32_16x16x128_f8f6f4 v[142:145], v[174:177], v[190:193], v[142:145] cbsz:4 blgp:4
	s_setprio 0
	s_barrier
	ds_read_b128 v[166:169], v161 offset:32768
	ds_read_b128 v[170:173], v161 offset:34816
	ds_read_b128 v[174:177], v162 offset:32768
	ds_read_b128 v[178:181], v162 offset:34816
	ds_read_b128 v[182:185], v163 offset:32768
	ds_read_b128 v[186:189], v163 offset:34816
	ds_read_b128 v[190:193], v164 offset:32768
	ds_read_b128 v[194:197], v164 offset:34816
	ds_read_b128 v[198:201], v163 offset:36864
	ds_read_b128 v[202:205], v163 offset:38912
	ds_read_b128 v[206:209], v164 offset:36864
	ds_read_b128 v[210:213], v164 offset:38912
	s_add_u32 s46, s46, s22
	s_addc_u32 s47, s47, s23
	s_mov_b32 m0, s60
	s_nop 0
	global_load_lds_dwordx4 v146, s[46:47] sc1
	s_mov_b32 m0, s61
	s_nop 0
	global_load_lds_dwordx4 v150, s[46:47] sc1
	s_waitcnt lgkmcnt(8)
	ds_read_b128 v[214:217], v161 offset:49152
	ds_read_b128 v[218:221], v161 offset:51200
	ds_read_b128 v[222:225], v162 offset:49152
	ds_read_b128 v[226:229], v162 offset:51200
	s_waitcnt vmcnt(8)
	s_waitcnt lgkmcnt(0)
	s_barrier
	s_waitcnt lgkmcnt(0)
	s_setprio 1
	v_mfma_f32_16x16x128_f8f6f4 v[18:21], v[166:169], v[182:185], v[18:21] cbsz:4 blgp:4
	v_mfma_f32_16x16x128_f8f6f4 v[18:21], v[174:177], v[190:193], v[18:21] cbsz:4 blgp:4
	v_mfma_f32_16x16x128_f8f6f4 v[22:25], v[170:173], v[182:185], v[22:25] cbsz:4 blgp:4
	v_mfma_f32_16x16x128_f8f6f4 v[22:25], v[178:181], v[190:193], v[22:25] cbsz:4 blgp:4
	v_mfma_f32_16x16x128_f8f6f4 v[26:29], v[166:169], v[186:189], v[26:29] cbsz:4 blgp:4
	v_mfma_f32_16x16x128_f8f6f4 v[26:29], v[174:177], v[194:197], v[26:29] cbsz:4 blgp:4
	v_mfma_f32_16x16x128_f8f6f4 v[30:33], v[170:173], v[186:189], v[30:33] cbsz:4 blgp:4
	v_mfma_f32_16x16x128_f8f6f4 v[30:33], v[178:181], v[194:197], v[30:33] cbsz:4 blgp:4
	v_mfma_f32_16x16x128_f8f6f4 v[34:37], v[166:169], v[198:201], v[34:37] cbsz:4 blgp:4
	v_mfma_f32_16x16x128_f8f6f4 v[34:37], v[174:177], v[206:209], v[34:37] cbsz:4 blgp:4
	v_mfma_f32_16x16x128_f8f6f4 v[38:41], v[170:173], v[198:201], v[38:41] cbsz:4 blgp:4
	v_mfma_f32_16x16x128_f8f6f4 v[38:41], v[178:181], v[206:209], v[38:41] cbsz:4 blgp:4
	v_mfma_f32_16x16x128_f8f6f4 v[42:45], v[166:169], v[202:205], v[42:45] cbsz:4 blgp:4
	v_mfma_f32_16x16x128_f8f6f4 v[42:45], v[174:177], v[210:213], v[42:45] cbsz:4 blgp:4
	v_mfma_f32_16x16x128_f8f6f4 v[46:49], v[170:173], v[202:205], v[46:49] cbsz:4 blgp:4
	v_mfma_f32_16x16x128_f8f6f4 v[46:49], v[178:181], v[210:213], v[46:49] cbsz:4 blgp:4
	v_mfma_f32_16x16x128_f8f6f4 v[50:53], v[214:217], v[182:185], v[50:53] cbsz:4 blgp:4
	v_mfma_f32_16x16x128_f8f6f4 v[50:53], v[222:225], v[190:193], v[50:53] cbsz:4 blgp:4
	v_mfma_f32_16x16x128_f8f6f4 v[54:57], v[218:221], v[182:185], v[54:57] cbsz:4 blgp:4
	v_mfma_f32_16x16x128_f8f6f4 v[54:57], v[226:229], v[190:193], v[54:57] cbsz:4 blgp:4
	v_mfma_f32_16x16x128_f8f6f4 v[58:61], v[214:217], v[186:189], v[58:61] cbsz:4 blgp:4
	v_mfma_f32_16x16x128_f8f6f4 v[58:61], v[222:225], v[194:197], v[58:61] cbsz:4 blgp:4
	v_mfma_f32_16x16x128_f8f6f4 v[62:65], v[218:221], v[186:189], v[62:65] cbsz:4 blgp:4
	v_mfma_f32_16x16x128_f8f6f4 v[62:65], v[226:229], v[194:197], v[62:65] cbsz:4 blgp:4
	v_mfma_f32_16x16x128_f8f6f4 v[66:69], v[214:217], v[198:201], v[66:69] cbsz:4 blgp:4
	v_mfma_f32_16x16x128_f8f6f4 v[66:69], v[222:225], v[206:209], v[66:69] cbsz:4 blgp:4
	v_mfma_f32_16x16x128_f8f6f4 v[70:73], v[218:221], v[198:201], v[70:73] cbsz:4 blgp:4
	v_mfma_f32_16x16x128_f8f6f4 v[70:73], v[226:229], v[206:209], v[70:73] cbsz:4 blgp:4
	v_mfma_f32_16x16x128_f8f6f4 v[74:77], v[214:217], v[202:205], v[74:77] cbsz:4 blgp:4
	v_mfma_f32_16x16x128_f8f6f4 v[74:77], v[222:225], v[210:213], v[74:77] cbsz:4 blgp:4
	v_mfma_f32_16x16x128_f8f6f4 v[78:81], v[218:221], v[202:205], v[78:81] cbsz:4 blgp:4
	v_mfma_f32_16x16x128_f8f6f4 v[78:81], v[226:229], v[210:213], v[78:81] cbsz:4 blgp:4
	s_setprio 0
	s_barrier
	s_mov_b32 m0, s64
	s_nop 0
	global_load_lds_dwordx4 v148, s[42:43] sc1
	s_mov_b32 m0, s65
	s_nop 0
	global_load_lds_dwordx4 v152, s[42:43] sc1
	ds_read_b128 v[182:185], v163 offset:49152
	ds_read_b128 v[186:189], v163 offset:51200
	ds_read_b128 v[190:193], v164 offset:49152
	ds_read_b128 v[194:197], v164 offset:51200
	ds_read_b128 v[198:201], v163 offset:53248
	ds_read_b128 v[202:205], v163 offset:55296
	ds_read_b128 v[206:209], v164 offset:53248
	ds_read_b128 v[210:213], v164 offset:55296
	s_mov_b32 m0, s66
	s_nop 0
	global_load_lds_dwordx4 v146, s[44:45] sc1
	s_mov_b32 m0, s67
	s_nop 0
	global_load_lds_dwordx4 v150, s[44:45] sc1
	s_add_u32 s42, s42, s24
	s_addc_u32 s43, s43, s25
	s_mov_b32 m0, s68
	s_nop 0
	global_load_lds_dwordx4 v148, s[42:43] sc1
	s_mov_b32 m0, s69
	s_nop 0
	global_load_lds_dwordx4 v152, s[42:43] sc1
	s_waitcnt vmcnt(8)
	s_waitcnt lgkmcnt(0)
	s_barrier
	s_setprio 1
	v_mfma_f32_16x16x128_f8f6f4 v[86:89], v[166:169], v[182:185], v[86:89] cbsz:4 blgp:4
	v_mfma_f32_16x16x128_f8f6f4 v[86:89], v[174:177], v[190:193], v[86:89] cbsz:4 blgp:4
	v_mfma_f32_16x16x128_f8f6f4 v[90:93], v[170:173], v[182:185], v[90:93] cbsz:4 blgp:4
	v_mfma_f32_16x16x128_f8f6f4 v[90:93], v[178:181], v[190:193], v[90:93] cbsz:4 blgp:4
	v_mfma_f32_16x16x128_f8f6f4 v[98:101], v[166:169], v[186:189], v[98:101] cbsz:4 blgp:4
	v_mfma_f32_16x16x128_f8f6f4 v[98:101], v[174:177], v[194:197], v[98:101] cbsz:4 blgp:4
	v_mfma_f32_16x16x128_f8f6f4 v[106:109], v[170:173], v[186:189], v[106:109] cbsz:4 blgp:4
	v_mfma_f32_16x16x128_f8f6f4 v[106:109], v[178:181], v[194:197], v[106:109] cbsz:4 blgp:4
	v_mfma_f32_16x16x128_f8f6f4 v[118:121], v[166:169], v[198:201], v[118:121] cbsz:4 blgp:4
	v_mfma_f32_16x16x128_f8f6f4 v[118:121], v[174:177], v[206:209], v[118:121] cbsz:4 blgp:4
	v_mfma_f32_16x16x128_f8f6f4 v[126:129], v[170:173], v[198:201], v[126:129] cbsz:4 blgp:4
	v_mfma_f32_16x16x128_f8f6f4 v[126:129], v[178:181], v[206:209], v[126:129] cbsz:4 blgp:4
	v_mfma_f32_16x16x128_f8f6f4 v[138:141], v[166:169], v[202:205], v[138:141] cbsz:4 blgp:4
	v_mfma_f32_16x16x128_f8f6f4 v[138:141], v[174:177], v[210:213], v[138:141] cbsz:4 blgp:4
	v_mfma_f32_16x16x128_f8f6f4 v[82:85], v[170:173], v[202:205], v[82:85] cbsz:4 blgp:4
	v_mfma_f32_16x16x128_f8f6f4 v[82:85], v[178:181], v[210:213], v[82:85] cbsz:4 blgp:4
	v_mfma_f32_16x16x128_f8f6f4 v[94:97], v[214:217], v[182:185], v[94:97] cbsz:4 blgp:4
	v_mfma_f32_16x16x128_f8f6f4 v[94:97], v[222:225], v[190:193], v[94:97] cbsz:4 blgp:4
	v_mfma_f32_16x16x128_f8f6f4 v[102:105], v[218:221], v[182:185], v[102:105] cbsz:4 blgp:4
	v_mfma_f32_16x16x128_f8f6f4 v[102:105], v[226:229], v[190:193], v[102:105] cbsz:4 blgp:4
	v_mfma_f32_16x16x128_f8f6f4 v[110:113], v[214:217], v[186:189], v[110:113] cbsz:4 blgp:4
	v_mfma_f32_16x16x128_f8f6f4 v[110:113], v[222:225], v[194:197], v[110:113] cbsz:4 blgp:4
	v_mfma_f32_16x16x128_f8f6f4 v[114:117], v[218:221], v[186:189], v[114:117] cbsz:4 blgp:4
	v_mfma_f32_16x16x128_f8f6f4 v[114:117], v[226:229], v[194:197], v[114:117] cbsz:4 blgp:4
	v_mfma_f32_16x16x128_f8f6f4 v[122:125], v[214:217], v[198:201], v[122:125] cbsz:4 blgp:4
	v_mfma_f32_16x16x128_f8f6f4 v[122:125], v[222:225], v[206:209], v[122:125] cbsz:4 blgp:4
	v_mfma_f32_16x16x128_f8f6f4 v[130:133], v[218:221], v[198:201], v[130:133] cbsz:4 blgp:4
	v_mfma_f32_16x16x128_f8f6f4 v[130:133], v[226:229], v[206:209], v[130:133] cbsz:4 blgp:4
	v_mfma_f32_16x16x128_f8f6f4 v[134:137], v[214:217], v[202:205], v[134:137] cbsz:4 blgp:4
	v_mfma_f32_16x16x128_f8f6f4 v[134:137], v[222:225], v[210:213], v[134:137] cbsz:4 blgp:4
	v_mfma_f32_16x16x128_f8f6f4 v[142:145], v[218:221], v[202:205], v[142:145] cbsz:4 blgp:4
	v_mfma_f32_16x16x128_f8f6f4 v[142:145], v[226:229], v[210:213], v[142:145] cbsz:4 blgp:4
	s_setprio 0
	s_andn2_b64 vcc, exec, s[34:35]
	s_barrier
	s_cbranch_vccnz .LBB4_4
	s_ashr_i32 s29, s28, 31
	s_lshl_b64 s[42:43], s[28:29], 10
	s_add_u32 s42, s10, s42
	s_addc_u32 s43, s11, s43
	s_add_u32 s29, s40, 0x200
	s_addc_u32 s78, s41, 0
	s_add_u32 s79, s38, 0x200
	s_addc_u32 s80, s39, 0
	s_add_u32 s38, s81, 0x180
	s_addc_u32 s39, s82, 0
	s_mov_b32 s81, 4
	s_cmp_eq_u32 s63, s81
	s_cselect_b64 s[40:41], -1, 0
	s_cmp_lg_u32 s63, s81
	s_cbranch_scc1 .LBB4_15

.LBB4_15:
	ds_read_b128 v[166:169], v161
	ds_read_b128 v[170:173], v161 offset:2048
	ds_read_b128 v[174:177], v162
	ds_read_b128 v[178:181], v162 offset:2048
	s_and_b64 s[40:41], s[40:41], exec
	s_cselect_b32 s46, s36, s29
	s_cselect_b32 s47, s37, s78
	s_cselect_b32 s49, s5, s80
	s_cselect_b32 s48, s4, s79
	s_add_u32 s44, s46, 0x80
	s_addc_u32 s45, s47, 0
	s_add_u32 s40, s48, 0x80
	s_addc_u32 s41, s49, 0
	ds_read_b128 v[182:185], v163
	ds_read_b128 v[186:189], v163 offset:2048
	ds_read_b128 v[190:193], v164
	ds_read_b128 v[194:197], v164 offset:2048
	ds_read_b128 v[198:201], v163 offset:4096
	ds_read_b128 v[202:205], v163 offset:6144
	ds_read_b128 v[206:209], v164 offset:4096
	ds_read_b128 v[210:213], v164 offset:6144
	s_mov_b32 m0, s70
	s_nop 0
	global_load_lds_dwordx4 v146, s[38:39] sc1
	s_mov_b32 m0, s71
	s_nop 0
	global_load_lds_dwordx4 v150, s[38:39] sc1
	s_waitcnt lgkmcnt(8)
	ds_read_b128 v[214:217], v161 offset:16384
	ds_read_b128 v[218:221], v161 offset:18432
	ds_read_b128 v[222:225], v162 offset:16384
	ds_read_b128 v[226:229], v162 offset:18432
	s_waitcnt vmcnt(8)
	s_waitcnt lgkmcnt(0)
	s_barrier
	s_waitcnt lgkmcnt(0)
	s_setprio 1
	v_mfma_f32_16x16x128_f8f6f4 v[18:21], v[166:169], v[182:185], v[18:21] cbsz:4 blgp:4
	v_mfma_f32_16x16x128_f8f6f4 v[18:21], v[174:177], v[190:193], v[18:21] cbsz:4 blgp:4
	v_mfma_f32_16x16x128_f8f6f4 v[22:25], v[170:173], v[182:185], v[22:25] cbsz:4 blgp:4
	v_mfma_f32_16x16x128_f8f6f4 v[22:25], v[178:181], v[190:193], v[22:25] cbsz:4 blgp:4
	v_mfma_f32_16x16x128_f8f6f4 v[26:29], v[166:169], v[186:189], v[26:29] cbsz:4 blgp:4
	v_mfma_f32_16x16x128_f8f6f4 v[26:29], v[174:177], v[194:197], v[26:29] cbsz:4 blgp:4
	v_mfma_f32_16x16x128_f8f6f4 v[30:33], v[170:173], v[186:189], v[30:33] cbsz:4 blgp:4
	v_mfma_f32_16x16x128_f8f6f4 v[30:33], v[178:181], v[194:197], v[30:33] cbsz:4 blgp:4
	v_mfma_f32_16x16x128_f8f6f4 v[34:37], v[166:169], v[198:201], v[34:37] cbsz:4 blgp:4
	v_mfma_f32_16x16x128_f8f6f4 v[34:37], v[174:177], v[206:209], v[34:37] cbsz:4 blgp:4
	v_mfma_f32_16x16x128_f8f6f4 v[38:41], v[170:173], v[198:201], v[38:41] cbsz:4 blgp:4
	v_mfma_f32_16x16x128_f8f6f4 v[38:41], v[178:181], v[206:209], v[38:41] cbsz:4 blgp:4
	v_mfma_f32_16x16x128_f8f6f4 v[42:45], v[166:169], v[202:205], v[42:45] cbsz:4 blgp:4
	v_mfma_f32_16x16x128_f8f6f4 v[42:45], v[174:177], v[210:213], v[42:45] cbsz:4 blgp:4
	v_mfma_f32_16x16x128_f8f6f4 v[46:49], v[170:173], v[202:205], v[46:49] cbsz:4 blgp:4
	v_mfma_f32_16x16x128_f8f6f4 v[46:49], v[178:181], v[210:213], v[46:49] cbsz:4 blgp:4
	v_mfma_f32_16x16x128_f8f6f4 v[50:53], v[214:217], v[182:185], v[50:53] cbsz:4 blgp:4
	v_mfma_f32_16x16x128_f8f6f4 v[50:53], v[222:225], v[190:193], v[50:53] cbsz:4 blgp:4
	v_mfma_f32_16x16x128_f8f6f4 v[54:57], v[218:221], v[182:185], v[54:57] cbsz:4 blgp:4
	v_mfma_f32_16x16x128_f8f6f4 v[54:57], v[226:229], v[190:193], v[54:57] cbsz:4 blgp:4
	v_mfma_f32_16x16x128_f8f6f4 v[58:61], v[214:217], v[186:189], v[58:61] cbsz:4 blgp:4
	v_mfma_f32_16x16x128_f8f6f4 v[58:61], v[222:225], v[194:197], v[58:61] cbsz:4 blgp:4
	v_mfma_f32_16x16x128_f8f6f4 v[62:65], v[218:221], v[186:189], v[62:65] cbsz:4 blgp:4
	v_mfma_f32_16x16x128_f8f6f4 v[62:65], v[226:229], v[194:197], v[62:65] cbsz:4 blgp:4
	v_mfma_f32_16x16x128_f8f6f4 v[66:69], v[214:217], v[198:201], v[66:69] cbsz:4 blgp:4
	v_mfma_f32_16x16x128_f8f6f4 v[66:69], v[222:225], v[206:209], v[66:69] cbsz:4 blgp:4
	v_mfma_f32_16x16x128_f8f6f4 v[70:73], v[218:221], v[198:201], v[70:73] cbsz:4 blgp:4
	v_mfma_f32_16x16x128_f8f6f4 v[70:73], v[226:229], v[206:209], v[70:73] cbsz:4 blgp:4
	v_mfma_f32_16x16x128_f8f6f4 v[74:77], v[214:217], v[202:205], v[74:77] cbsz:4 blgp:4
	v_mfma_f32_16x16x128_f8f6f4 v[74:77], v[222:225], v[210:213], v[74:77] cbsz:4 blgp:4
	v_mfma_f32_16x16x128_f8f6f4 v[78:81], v[218:221], v[202:205], v[78:81] cbsz:4 blgp:4
	v_mfma_f32_16x16x128_f8f6f4 v[78:81], v[226:229], v[210:213], v[78:81] cbsz:4 blgp:4
	s_setprio 0
	s_barrier
	s_mov_b32 m0, s55
	s_nop 0
	global_load_lds_dwordx4 v148, s[48:49] sc1
	s_mov_b32 m0, s56
	s_nop 0
	global_load_lds_dwordx4 v152, s[48:49] sc1
	ds_read_b128 v[182:185], v163 offset:16384
	ds_read_b128 v[186:189], v163 offset:18432
	ds_read_b128 v[190:193], v164 offset:16384
	ds_read_b128 v[194:197], v164 offset:18432
	ds_read_b128 v[198:201], v163 offset:20480
	ds_read_b128 v[202:205], v163 offset:22528
	ds_read_b128 v[206:209], v164 offset:20480
	ds_read_b128 v[210:213], v164 offset:22528
	s_mov_b32 m0, s54
	s_nop 0
	global_load_lds_dwordx4 v146, s[46:47] sc1
	s_mov_b32 m0, s57
	s_nop 0
	global_load_lds_dwordx4 v150, s[46:47] sc1
	s_add_u32 s48, s48, s24
	s_addc_u32 s49, s49, s25
	s_mov_b32 m0, s58
	s_nop 0
	global_load_lds_dwordx4 v148, s[48:49] sc1
	s_mov_b32 m0, s59
	s_nop 0
	global_load_lds_dwordx4 v152, s[48:49] sc1
	s_waitcnt vmcnt(8)
	s_waitcnt lgkmcnt(0)
	s_barrier
	s_setprio 1
	v_mfma_f32_16x16x128_f8f6f4 v[86:89], v[166:169], v[182:185], v[86:89] cbsz:4 blgp:4
	v_mfma_f32_16x16x128_f8f6f4 v[86:89], v[174:177], v[190:193], v[86:89] cbsz:4 blgp:4
	v_mfma_f32_16x16x128_f8f6f4 v[90:93], v[170:173], v[182:185], v[90:93] cbsz:4 blgp:4
	v_mfma_f32_16x16x128_f8f6f4 v[90:93], v[178:181], v[190:193], v[90:93] cbsz:4 blgp:4
	v_mfma_f32_16x16x128_f8f6f4 v[98:101], v[166:169], v[186:189], v[98:101] cbsz:4 blgp:4
	v_mfma_f32_16x16x128_f8f6f4 v[98:101], v[174:177], v[194:197], v[98:101] cbsz:4 blgp:4
	v_mfma_f32_16x16x128_f8f6f4 v[106:109], v[170:173], v[186:189], v[106:109] cbsz:4 blgp:4
	v_mfma_f32_16x16x128_f8f6f4 v[106:109], v[178:181], v[194:197], v[106:109] cbsz:4 blgp:4
	v_mfma_f32_16x16x128_f8f6f4 v[118:121], v[166:169], v[198:201], v[118:121] cbsz:4 blgp:4
	v_mfma_f32_16x16x128_f8f6f4 v[118:121], v[174:177], v[206:209], v[118:121] cbsz:4 blgp:4
	v_mfma_f32_16x16x128_f8f6f4 v[126:129], v[170:173], v[198:201], v[126:129] cbsz:4 blgp:4
	v_mfma_f32_16x16x128_f8f6f4 v[126:129], v[178:181], v[206:209], v[126:129] cbsz:4 blgp:4
	v_mfma_f32_16x16x128_f8f6f4 v[138:141], v[166:169], v[202:205], v[138:141] cbsz:4 blgp:4
	v_mfma_f32_16x16x128_f8f6f4 v[138:141], v[174:177], v[210:213], v[138:141] cbsz:4 blgp:4
	v_mfma_f32_16x16x128_f8f6f4 v[82:85], v[170:173], v[202:205], v[82:85] cbsz:4 blgp:4
	v_mfma_f32_16x16x128_f8f6f4 v[82:85], v[178:181], v[210:213], v[82:85] cbsz:4 blgp:4
	v_mfma_f32_16x16x128_f8f6f4 v[94:97], v[214:217], v[182:185], v[94:97] cbsz:4 blgp:4
	v_mfma_f32_16x16x128_f8f6f4 v[94:97], v[222:225], v[190:193], v[94:97] cbsz:4 blgp:4
	v_mfma_f32_16x16x128_f8f6f4 v[102:105], v[218:221], v[182:185], v[102:105] cbsz:4 blgp:4
	v_mfma_f32_16x16x128_f8f6f4 v[102:105], v[226:229], v[190:193], v[102:105] cbsz:4 blgp:4
	v_mfma_f32_16x16x128_f8f6f4 v[110:113], v[214:217], v[186:189], v[110:113] cbsz:4 blgp:4
	v_mfma_f32_16x16x128_f8f6f4 v[110:113], v[222:225], v[194:197], v[110:113] cbsz:4 blgp:4
	v_mfma_f32_16x16x128_f8f6f4 v[114:117], v[218:221], v[186:189], v[114:117] cbsz:4 blgp:4
	v_mfma_f32_16x16x128_f8f6f4 v[114:117], v[226:229], v[194:197], v[114:117] cbsz:4 blgp:4
	v_mfma_f32_16x16x128_f8f6f4 v[122:125], v[214:217], v[198:201], v[122:125] cbsz:4 blgp:4
	v_mfma_f32_16x16x128_f8f6f4 v[122:125], v[222:225], v[206:209], v[122:125] cbsz:4 blgp:4
	v_mfma_f32_16x16x128_f8f6f4 v[130:133], v[218:221], v[198:201], v[130:133] cbsz:4 blgp:4
	v_mfma_f32_16x16x128_f8f6f4 v[130:133], v[226:229], v[206:209], v[130:133] cbsz:4 blgp:4
	v_mfma_f32_16x16x128_f8f6f4 v[134:137], v[214:217], v[202:205], v[134:137] cbsz:4 blgp:4
	v_mfma_f32_16x16x128_f8f6f4 v[134:137], v[222:225], v[210:213], v[134:137] cbsz:4 blgp:4
	v_mfma_f32_16x16x128_f8f6f4 v[142:145], v[218:221], v[202:205], v[142:145] cbsz:4 blgp:4
	v_mfma_f32_16x16x128_f8f6f4 v[142:145], v[226:229], v[210:213], v[142:145] cbsz:4 blgp:4
	s_setprio 0
	s_barrier
	ds_read_b128 v[166:169], v161 offset:32768
	ds_read_b128 v[170:173], v161 offset:34816
	ds_read_b128 v[174:177], v162 offset:32768
	ds_read_b128 v[178:181], v162 offset:34816
	ds_read_b128 v[182:185], v163 offset:32768
	ds_read_b128 v[186:189], v163 offset:34816
	ds_read_b128 v[190:193], v164 offset:32768
	ds_read_b128 v[194:197], v164 offset:34816
	ds_read_b128 v[198:201], v163 offset:36864
	ds_read_b128 v[202:205], v163 offset:38912
	ds_read_b128 v[206:209], v164 offset:36864
	ds_read_b128 v[210:213], v164 offset:38912
	s_add_u32 s46, s46, s22
	s_addc_u32 s47, s47, s23
	s_mov_b32 m0, s60
	s_nop 0
	global_load_lds_dwordx4 v146, s[46:47] sc1
	s_mov_b32 m0, s61
	s_nop 0
	global_load_lds_dwordx4 v150, s[46:47] sc1
	s_waitcnt lgkmcnt(8)
	ds_read_b128 v[214:217], v161 offset:49152
	ds_read_b128 v[218:221], v161 offset:51200
	ds_read_b128 v[222:225], v162 offset:49152
	ds_read_b128 v[226:229], v162 offset:51200
	s_waitcnt vmcnt(8)
	s_waitcnt lgkmcnt(0)
	s_barrier
	s_waitcnt lgkmcnt(0)
	s_setprio 1
	v_mfma_f32_16x16x128_f8f6f4 v[18:21], v[166:169], v[182:185], v[18:21] cbsz:4 blgp:4
	v_mfma_f32_16x16x128_f8f6f4 v[18:21], v[174:177], v[190:193], v[18:21] cbsz:4 blgp:4
	v_mfma_f32_16x16x128_f8f6f4 v[22:25], v[170:173], v[182:185], v[22:25] cbsz:4 blgp:4
	v_mfma_f32_16x16x128_f8f6f4 v[22:25], v[178:181], v[190:193], v[22:25] cbsz:4 blgp:4
	v_mfma_f32_16x16x128_f8f6f4 v[26:29], v[166:169], v[186:189], v[26:29] cbsz:4 blgp:4
	v_mfma_f32_16x16x128_f8f6f4 v[26:29], v[174:177], v[194:197], v[26:29] cbsz:4 blgp:4
	v_mfma_f32_16x16x128_f8f6f4 v[30:33], v[170:173], v[186:189], v[30:33] cbsz:4 blgp:4
	v_mfma_f32_16x16x128_f8f6f4 v[30:33], v[178:181], v[194:197], v[30:33] cbsz:4 blgp:4
	v_mfma_f32_16x16x128_f8f6f4 v[34:37], v[166:169], v[198:201], v[34:37] cbsz:4 blgp:4
	v_mfma_f32_16x16x128_f8f6f4 v[34:37], v[174:177], v[206:209], v[34:37] cbsz:4 blgp:4
	v_mfma_f32_16x16x128_f8f6f4 v[38:41], v[170:173], v[198:201], v[38:41] cbsz:4 blgp:4
	v_mfma_f32_16x16x128_f8f6f4 v[38:41], v[178:181], v[206:209], v[38:41] cbsz:4 blgp:4
	v_mfma_f32_16x16x128_f8f6f4 v[42:45], v[166:169], v[202:205], v[42:45] cbsz:4 blgp:4
	v_mfma_f32_16x16x128_f8f6f4 v[42:45], v[174:177], v[210:213], v[42:45] cbsz:4 blgp:4
	v_mfma_f32_16x16x128_f8f6f4 v[46:49], v[170:173], v[202:205], v[46:49] cbsz:4 blgp:4
	v_mfma_f32_16x16x128_f8f6f4 v[46:49], v[178:181], v[210:213], v[46:49] cbsz:4 blgp:4
	v_mfma_f32_16x16x128_f8f6f4 v[50:53], v[214:217], v[182:185], v[50:53] cbsz:4 blgp:4
	v_mfma_f32_16x16x128_f8f6f4 v[50:53], v[222:225], v[190:193], v[50:53] cbsz:4 blgp:4
	v_mfma_f32_16x16x128_f8f6f4 v[54:57], v[218:221], v[182:185], v[54:57] cbsz:4 blgp:4
	v_mfma_f32_16x16x128_f8f6f4 v[54:57], v[226:229], v[190:193], v[54:57] cbsz:4 blgp:4
	v_mfma_f32_16x16x128_f8f6f4 v[58:61], v[214:217], v[186:189], v[58:61] cbsz:4 blgp:4
	v_mfma_f32_16x16x128_f8f6f4 v[58:61], v[222:225], v[194:197], v[58:61] cbsz:4 blgp:4
	v_mfma_f32_16x16x128_f8f6f4 v[62:65], v[218:221], v[186:189], v[62:65] cbsz:4 blgp:4
	v_mfma_f32_16x16x128_f8f6f4 v[62:65], v[226:229], v[194:197], v[62:65] cbsz:4 blgp:4
	v_mfma_f32_16x16x128_f8f6f4 v[66:69], v[214:217], v[198:201], v[66:69] cbsz:4 blgp:4
	v_mfma_f32_16x16x128_f8f6f4 v[66:69], v[222:225], v[206:209], v[66:69] cbsz:4 blgp:4
	v_mfma_f32_16x16x128_f8f6f4 v[70:73], v[218:221], v[198:201], v[70:73] cbsz:4 blgp:4
	v_mfma_f32_16x16x128_f8f6f4 v[70:73], v[226:229], v[206:209], v[70:73] cbsz:4 blgp:4
	v_mfma_f32_16x16x128_f8f6f4 v[74:77], v[214:217], v[202:205], v[74:77] cbsz:4 blgp:4
	v_mfma_f32_16x16x128_f8f6f4 v[74:77], v[222:225], v[210:213], v[74:77] cbsz:4 blgp:4
	v_mfma_f32_16x16x128_f8f6f4 v[78:81], v[218:221], v[202:205], v[78:81] cbsz:4 blgp:4
	v_mfma_f32_16x16x128_f8f6f4 v[78:81], v[226:229], v[210:213], v[78:81] cbsz:4 blgp:4
	s_setprio 0
	s_barrier
	s_mov_b32 m0, s64
	s_nop 0
	global_load_lds_dwordx4 v148, s[40:41] sc1
	s_mov_b32 m0, s65
	s_nop 0
	global_load_lds_dwordx4 v152, s[40:41] sc1
	ds_read_b128 v[182:185], v163 offset:49152
	ds_read_b128 v[186:189], v163 offset:51200
	ds_read_b128 v[190:193], v164 offset:49152
	ds_read_b128 v[194:197], v164 offset:51200
	ds_read_b128 v[198:201], v163 offset:53248
	ds_read_b128 v[202:205], v163 offset:55296
	ds_read_b128 v[206:209], v164 offset:53248
	ds_read_b128 v[210:213], v164 offset:55296
	s_mov_b32 m0, s66
	s_nop 0
	global_load_lds_dwordx4 v146, s[44:45] sc1
	s_mov_b32 m0, s67
	s_nop 0
	global_load_lds_dwordx4 v150, s[44:45] sc1
	s_add_u32 s40, s40, s24
	s_addc_u32 s41, s41, s25
	s_mov_b32 m0, s68
	s_nop 0
	global_load_lds_dwordx4 v148, s[40:41] sc1
	s_mov_b32 m0, s69
	s_nop 0
	global_load_lds_dwordx4 v152, s[40:41] sc1
	s_waitcnt vmcnt(8)
	s_waitcnt lgkmcnt(0)
	s_barrier
	s_setprio 1
	v_mfma_f32_16x16x128_f8f6f4 v[86:89], v[166:169], v[182:185], v[86:89] cbsz:4 blgp:4
	v_mfma_f32_16x16x128_f8f6f4 v[86:89], v[174:177], v[190:193], v[86:89] cbsz:4 blgp:4
	v_mfma_f32_16x16x128_f8f6f4 v[90:93], v[170:173], v[182:185], v[90:93] cbsz:4 blgp:4
	v_mfma_f32_16x16x128_f8f6f4 v[90:93], v[178:181], v[190:193], v[90:93] cbsz:4 blgp:4
	v_mfma_f32_16x16x128_f8f6f4 v[98:101], v[166:169], v[186:189], v[98:101] cbsz:4 blgp:4
	v_mfma_f32_16x16x128_f8f6f4 v[98:101], v[174:177], v[194:197], v[98:101] cbsz:4 blgp:4
	v_mfma_f32_16x16x128_f8f6f4 v[106:109], v[170:173], v[186:189], v[106:109] cbsz:4 blgp:4
	v_mfma_f32_16x16x128_f8f6f4 v[106:109], v[178:181], v[194:197], v[106:109] cbsz:4 blgp:4
	v_mfma_f32_16x16x128_f8f6f4 v[118:121], v[166:169], v[198:201], v[118:121] cbsz:4 blgp:4
	v_mfma_f32_16x16x128_f8f6f4 v[118:121], v[174:177], v[206:209], v[118:121] cbsz:4 blgp:4
	v_mfma_f32_16x16x128_f8f6f4 v[126:129], v[170:173], v[198:201], v[126:129] cbsz:4 blgp:4
	v_mfma_f32_16x16x128_f8f6f4 v[126:129], v[178:181], v[206:209], v[126:129] cbsz:4 blgp:4
	v_mfma_f32_16x16x128_f8f6f4 v[138:141], v[166:169], v[202:205], v[138:141] cbsz:4 blgp:4
	v_mfma_f32_16x16x128_f8f6f4 v[138:141], v[174:177], v[210:213], v[138:141] cbsz:4 blgp:4
	v_mfma_f32_16x16x128_f8f6f4 v[82:85], v[170:173], v[202:205], v[82:85] cbsz:4 blgp:4
	v_mfma_f32_16x16x128_f8f6f4 v[82:85], v[178:181], v[210:213], v[82:85] cbsz:4 blgp:4
	v_mfma_f32_16x16x128_f8f6f4 v[94:97], v[214:217], v[182:185], v[94:97] cbsz:4 blgp:4
	v_mfma_f32_16x16x128_f8f6f4 v[94:97], v[222:225], v[190:193], v[94:97] cbsz:4 blgp:4
	v_mfma_f32_16x16x128_f8f6f4 v[102:105], v[218:221], v[182:185], v[102:105] cbsz:4 blgp:4
	v_mfma_f32_16x16x128_f8f6f4 v[102:105], v[226:229], v[190:193], v[102:105] cbsz:4 blgp:4
	v_mfma_f32_16x16x128_f8f6f4 v[110:113], v[214:217], v[186:189], v[110:113] cbsz:4 blgp:4
	v_mfma_f32_16x16x128_f8f6f4 v[110:113], v[222:225], v[194:197], v[110:113] cbsz:4 blgp:4
	v_mfma_f32_16x16x128_f8f6f4 v[114:117], v[218:221], v[186:189], v[114:117] cbsz:4 blgp:4
	v_mfma_f32_16x16x128_f8f6f4 v[114:117], v[226:229], v[194:197], v[114:117] cbsz:4 blgp:4
	v_mfma_f32_16x16x128_f8f6f4 v[122:125], v[214:217], v[198:201], v[122:125] cbsz:4 blgp:4
	v_mfma_f32_16x16x128_f8f6f4 v[122:125], v[222:225], v[206:209], v[122:125] cbsz:4 blgp:4
	v_mfma_f32_16x16x128_f8f6f4 v[130:133], v[218:221], v[198:201], v[130:133] cbsz:4 blgp:4
	v_mfma_f32_16x16x128_f8f6f4 v[130:133], v[226:229], v[206:209], v[130:133] cbsz:4 blgp:4
	v_mfma_f32_16x16x128_f8f6f4 v[134:137], v[214:217], v[202:205], v[134:137] cbsz:4 blgp:4
	v_mfma_f32_16x16x128_f8f6f4 v[134:137], v[222:225], v[210:213], v[134:137] cbsz:4 blgp:4
	v_mfma_f32_16x16x128_f8f6f4 v[142:145], v[218:221], v[202:205], v[142:145] cbsz:4 blgp:4
	v_mfma_f32_16x16x128_f8f6f4 v[142:145], v[226:229], v[210:213], v[142:145] cbsz:4 blgp:4
	s_setprio 0
	s_add_i32 s40, s81, 2
	s_add_u32 s29, s29, 0x100
	s_addc_u32 s78, s78, 0
	s_add_u32 s79, s79, 0x100
	s_addc_u32 s80, s80, 0
	s_add_u32 s38, s38, 0x100
	s_addc_u32 s39, s39, 0
	s_cmp_ge_i32 s81, s63
	s_barrier
	s_cbranch_scc1 .LBB4_4
	s_mov_b32 s81, s40
	s_cmp_eq_u32 s63, s81
	s_cselect_b64 s[40:41], -1, 0
	s_cmp_lg_u32 s63, s81
	s_cbranch_scc0 .LBB4_14
	s_branch .LBB4_15

_Z6k_gemmI4Epi8ILi1ELb1ELb1EEEv4GemmT_iiii:
	s_load_dwordx4 s[4:7], s[0:1], 0x38
	s_waitcnt lgkmcnt(0)
	s_mul_i32 s3, s5, s4
	s_mul_i32 s20, s3, s6
	s_cmp_ge_i32 s2, s20
	v_readfirstlane_b32 s3, v0
	s_cbranch_scc1 .LBB5_20
	s_ashr_i32 s21, s20, 31
	s_load_dword s34, s[0:1], 0x10
	s_load_dwordx4 s[16:19], s[0:1], 0x0
	s_load_dwordx8 s[8:15], s[0:1], 0x18
	s_load_dword s33, s[0:1], 0x48
	s_lshr_b32 s0, s21, 29
	v_lshrrev_b32_e32 v5, 5, v0
	s_add_i32 s0, s20, s0
	v_lshlrev_b32_e32 v3, 4, v0
	v_and_b32_e32 v5, 4, v5
	v_lshrrev_b32_e32 v6, 3, v0
	v_lshrrev_b32_e32 v7, 2, v0
	v_lshrrev_b32_e32 v18, 1, v0
	v_lshlrev_b32_e32 v9, 1, v0
	s_ashr_i32 s0, s0, 3
	v_and_b32_e32 v2, 16, v0
	v_and_b32_e32 v4, 0x70, v3
	v_and_b32_e32 v7, 64, v7
	v_and_or_b32 v5, v6, 3, v5
	v_and_b32_e32 v8, 48, v18
	v_and_b32_e32 v9, 64, v9
	s_ff1_i32_b32 s37, s0
	s_lshl_b32 s0, s6, 3
	v_or3_b32 v7, v8, v7, v5
	v_bitop3_b32 v2, v9, v4, v2 bitop3:0x36
	s_ff1_i32_b32 s52, s0
	s_waitcnt lgkmcnt(0)
	v_mad_u64_u32 v[146:147], s[0:1], s34, v6, v[2:3]
	v_mad_u64_u32 v[148:149], s[0:1], s34, v7, v[2:3]
	v_or_b32_e32 v3, 0x2000, v3
	v_lshrrev_b32_e32 v4, 7, v3
	v_lshrrev_b32_e32 v3, 6, v3
	v_and_b32_e32 v3, 0xc0, v3
	v_or3_b32 v3, v8, v3, v5
	s_lshr_b32 s28, s3, 6
	v_mad_u64_u32 v[150:151], s[0:1], s34, v4, v[2:3]
	v_mad_u64_u32 v[152:153], s[0:1], s34, v3, v[2:3]
	s_lshl_b32 s0, s28, 10
	s_add_i32 s55, s0, 0
	s_and_b32 s0, s2, 7
	s_lshl_b32 s0, s0, s37
	s_ashr_i32 s1, s2, 3
	s_add_i32 s0, s0, s1
	s_lshl_b32 s30, -1, s52
	s_ashr_i32 s1, s0, s52
	s_andn2_b32 s0, s0, s30
	s_lshl_b32 s1, s1, 3
	s_and_b32 s28, s0, 7
	s_ashr_i32 s35, s34, 31
	s_ff1_i32_b32 s53, s5
	s_or_b32 s78, s1, s28
	s_bfe_u32 s4, s3, 0x20006
	s_lshr_b32 s15, s3, 8
	s_lshl_b64 s[22:23], s[34:35], 7
	s_lshl_b64 s[24:25], s[34:35], 3
	s_lshl_b64 s[26:27], s[34:35], 8
	s_lshr_b32 s77, s0, 3
	s_ashr_i32 s0, s78, s53
	s_add_i32 s1, s5, -1
	s_cmp_lg_u32 s7, 0
	s_cselect_b32 s7, s1, -1
	s_and_b32 s5, s78, s7
	s_mul_i32 s0, s0, s6
	s_add_i32 s28, s0, s77
	s_ashr_i32 s0, s5, 31
	s_mul_i32 s0, s26, s0
	s_mul_hi_u32 s1, s26, s5
	s_add_i32 s29, s1, s0
	s_lshr_b64 s[0:1], s[34:35], 24
	s_mul_i32 s1, s0, s5
	s_add_i32 s31, s29, s1
	s_ashr_i32 s29, s28, 31
	s_mul_i32 s36, s26, s5
	s_mul_i32 s1, s26, s29
	s_mul_hi_u32 s5, s26, s28
	s_add_i32 s1, s5, s1
	s_mul_i32 s0, s0, s28
	s_add_i32 s1, s1, s0
	s_mul_i32 s0, s26, s28
	s_add_u32 s40, s18, s0
	v_bfe_u32 v1, v0, 4, 2
	s_addc_u32 s41, s19, s1
	s_lshl_b64 s[0:1], s[28:29], 10
	v_lshlrev_b32_e32 v2, 6, v1
	s_add_u32 s0, s10, s0
	v_lshl_or_b32 v147, s4, 8, v2
	s_addc_u32 s1, s11, s1
	global_load_dwordx4 v[14:17], v147, s[0:1]
	global_load_dwordx4 v[10:13], v147, s[0:1] offset:16
	global_load_dwordx4 v[6:9], v147, s[0:1] offset:32
	global_load_dwordx4 v[2:5], v147, s[0:1] offset:48
	s_add_i32 s56, s55, 0x10000
	s_mov_b32 m0, s56
	s_nop 0
	global_load_lds_dwordx4 v148, s[40:41] sc1
	s_add_i32 s57, s55, 0x12000
	s_mov_b32 m0, s57
	s_nop 0
	global_load_lds_dwordx4 v152, s[40:41] sc1
	s_add_u32 s42, s16, s36
	s_addc_u32 s43, s17, s31
	s_mov_b32 m0, s55
	s_nop 0
	global_load_lds_dwordx4 v146, s[42:43] sc1
	s_add_i32 s58, s55, 0x2000
	s_add_i32 s59, s55, 0x14000
	s_mov_b32 m0, s58
	s_nop 0
	global_load_lds_dwordx4 v150, s[42:43] sc1
	s_add_u32 s0, s40, s24
	s_addc_u32 s1, s41, s25
	s_mov_b32 m0, s59
	s_nop 0
	global_load_lds_dwordx4 v148, s[0:1] sc1
	s_add_i32 s60, s55, 0x16000
	s_add_i32 s61, s55, 0x4000
	s_mov_b32 m0, s60
	s_nop 0
	global_load_lds_dwordx4 v152, s[0:1] sc1
	s_add_u32 s38, s42, s22
	s_addc_u32 s39, s43, s23
	s_mov_b32 m0, s61
	s_nop 0
	global_load_lds_dwordx4 v146, s[38:39] sc1
	s_add_i32 s62, s55, 0x6000
	s_mov_b32 m0, s62
	s_nop 0
	global_load_lds_dwordx4 v150, s[38:39] sc1
	s_mov_b32 s54, 0
	s_mov_b32 s5, 0x10000
	s_cmp_lg_u32 s15, 1
	s_cbranch_scc1 .LBB5_3
.LBB5_3:
	s_lshr_b32 s29, s35, 25
	s_add_i32 s29, s34, s29
	s_not_b32 s63, s30
	s_ashr_i32 s64, s29, 7
	s_add_i32 s65, s55, 0x18000
	v_and_b32_e32 v19, 15, v0
	v_and_b32_e32 v0, 4, v0
	s_add_u32 s30, s40, 0x80
	v_lshl_or_b32 v149, s15, 6, v19
	v_lshlrev_b32_e32 v20, 5, v1
	v_and_or_b32 v0, v18, 1, v0
	s_waitcnt vmcnt(0)
	s_barrier
	s_addc_u32 s31, s41, 0
	s_mov_b32 m0, s65
	s_nop 0
	global_load_lds_dwordx4 v148, s[30:31] sc1
	s_add_i32 s66, s55, 0x1a000
	s_add_i32 s67, s55, 0x8000
	v_lshlrev_b32_e32 v21, 7, v149
	v_lshlrev_b32_e32 v0, 4, v0
	v_or_b32_e32 v23, 16, v20
	s_mov_b32 m0, s66
	s_nop 0
	global_load_lds_dwordx4 v152, s[30:31] sc1
	s_add_u32 s30, s42, 0x80
	v_xor_b32_e32 v18, v0, v20
	v_bitop3_b32 v22, v21, v0, v20 bitop3:0xf6
	v_bitop3_b32 v20, v0, v20, 16 bitop3:0x1e
	v_bitop3_b32 v21, v21, v0, v23 bitop3:0xf6
	v_lshlrev_b32_e32 v0, 7, v19
	s_addc_u32 s31, s43, 0
	s_mov_b32 m0, s67
	s_nop 0
	global_load_lds_dwordx4 v146, s[30:31] sc1
	s_add_i32 s68, s55, 0xa000
	s_add_i32 s69, s55, 0x1c000
	v_lshl_or_b32 v0, s4, 12, v0
	s_mov_b32 m0, s68
	s_nop 0
	global_load_lds_dwordx4 v150, s[30:31] sc1
	s_add_u32 s0, s0, 0x80
	v_or3_b32 v18, v18, v0, s5
	v_or3_b32 v19, v20, v0, s5
	s_addc_u32 s1, s1, 0
	s_mov_b32 m0, s69
	s_nop 0
	global_load_lds_dwordx4 v148, s[0:1] sc1
	v_lshlrev_b32_e32 v0, 4, v1
	s_add_i32 s70, s55, 0x1e000
	s_mov_b32 m0, s70
	s_nop 0
	global_load_lds_dwordx4 v152, s[0:1] sc1
	v_and_b32_e32 v1, 32, v0
	v_and_b32_e32 v153, 16, v0
	v_or_b32_e32 v160, 32, v0
	v_div_scale_f32 v0, s[0:1], s13, s13, 1.0
	v_lshl_or_b32 v151, s4, 6, v1
	v_rcp_f32_e32 v1, v0
	s_cmpk_gt_i32 s34, 0x7f
	s_cselect_b64 s[30:31], -1, 0
	s_add_i32 s71, s55, 0xc000
	v_fma_f32 v20, -v0, v1, 1.0
	v_fmac_f32_e32 v1, v20, v1
	v_div_scale_f32 v20, vcc, 1.0, s13, 1.0
	v_mul_f32_e32 v23, v20, v1
	v_fma_f32 v24, -v0, v23, v20
	v_fmac_f32_e32 v23, v24, v1
	v_fma_f32 v0, -v0, v23, v20
	v_div_fmas_f32 v0, v0, v1, v23
	v_mov_b32_e32 v1, s14
	v_mul_f32_e32 v1, s13, v1
	v_div_scale_f32 v20, s[0:1], v1, v1, 1.0
	v_rcp_f32_e32 v23, v20
	s_add_i32 s72, s55, 0xe000
	s_ashr_i32 s73, s33, 31
	s_ashr_i32 s74, s2, 31
	v_fma_f32 v24, -v20, v23, 1.0
	v_fmac_f32_e32 v23, v24, v23
	v_div_scale_f32 v24, vcc, 1.0, v1, 1.0
	v_mul_f32_e32 v25, v24, v23
	v_fma_f32 v26, -v20, v25, v24
	v_fmac_f32_e32 v25, v26, v23
	v_fma_f32 v20, -v20, v25, v24
	s_waitcnt vmcnt(6)
	v_div_fmas_f32 v20, v20, v23, v25
	s_cmp_eq_u32 s64, 2
	v_div_fixup_f32 v0, v0, s13, 1.0
	v_div_fixup_f32 v161, v20, v1, 1.0
	s_cselect_b64 s[14:15], -1, 0
	s_cmpk_gt_u32 s34, 0x17f
	v_mov_b32_e32 v154, v0
	v_mov_b32_e32 v155, v0
	v_mul_f32_e32 v162, 0x40c00000, v161
	s_cselect_b64 s[34:35], -1, 0
	s_mov_b32 s36, 0x3c23d70a
	v_add_u32_e32 v163, 0, v18
	v_add_u32_e32 v164, 0, v19
	v_add_u32_e32 v165, 0, v22
	v_add_u32_e32 v166, 0, v21
	s_barrier
	s_branch .LBB5_5

.Lrs_a_5:
	s_add_u32 s82, s42, s22
	s_addc_u32 s83, s43, s23
	s_add_u32 s29, s42, 0x100
	s_addc_u32 s46, s43, 0
	s_and_b64 s[44:45], s[14:15], exec
	ds_read_b128 v[82:85], v163
	ds_read_b128 v[94:97], v163 offset:2048
	ds_read_b128 v[102:105], v164
	ds_read_b128 v[110:113], v164 offset:2048
	s_cselect_b32 s49, s39, s46
	s_cselect_b32 s48, s38, s29
	s_add_u32 s29, s40, 0x100
	s_addc_u32 s46, s41, 0
	s_and_b64 s[44:45], s[14:15], exec
	s_cselect_b32 s51, s5, s46
	s_cselect_b32 s50, s4, s29
	s_add_u32 s46, s48, 0x80
	s_addc_u32 s47, s49, 0
	s_add_u32 s44, s50, 0x80
	s_addc_u32 s45, s51, 0
	ds_read_b128 v[58:61], v165
	ds_read_b128 v[66:69], v165 offset:2048
	ds_read_b128 v[62:65], v166
	ds_read_b128 v[70:73], v166 offset:2048
	ds_read_b128 v[74:77], v165 offset:4096
	ds_read_b128 v[86:89], v165 offset:6144
	ds_read_b128 v[78:81], v166 offset:4096
	ds_read_b128 v[90:93], v166 offset:6144
	s_add_u32 s80, s82, 0x80
	s_addc_u32 s81, s83, 0
	s_mov_b32 m0, s71
	s_nop 0
	global_load_lds_dwordx4 v146, s[80:81] sc1
	s_mov_b32 m0, s72
	s_nop 0
	global_load_lds_dwordx4 v150, s[80:81] sc1
	s_waitcnt lgkmcnt(8)
	ds_read_b128 v[142:145], v163 offset:16384
	ds_read_b128 v[156:159], v163 offset:18432
	ds_read_b128 v[168:171], v164 offset:16384
	ds_read_b128 v[172:175], v164 offset:18432
	s_waitcnt vmcnt(8)
	s_waitcnt lgkmcnt(0)
	s_barrier
	s_waitcnt lgkmcnt(0)
	s_waitcnt vmcnt(16)
	v_mov_b32_e32 v1, v0
	v_pk_mul_f32 v[16:17], v[0:1], v[16:17]
	v_pk_mul_f32 v[14:15], v[154:155], v[14:15]
	v_pk_mul_f32 v[12:13], v[0:1], v[12:13]
	v_pk_mul_f32 v[10:11], v[154:155], v[10:11]
	v_pk_mul_f32 v[8:9], v[0:1], v[8:9]
	v_pk_mul_f32 v[6:7], v[154:155], v[6:7]
	v_pk_mul_f32 v[4:5], v[0:1], v[4:5]
	v_pk_mul_f32 v[2:3], v[154:155], v[2:3]
	s_setprio 1
	v_mfma_f32_16x16x128_f8f6f4 v[18:21], v[82:85], v[58:61], v[14:17] cbsz:4 blgp:4
	v_mfma_f32_16x16x128_f8f6f4 v[18:21], v[102:105], v[62:65], v[18:21] cbsz:4 blgp:4
	v_mfma_f32_16x16x128_f8f6f4 v[22:25], v[94:97], v[58:61], v[10:13] cbsz:4 blgp:4
	v_mfma_f32_16x16x128_f8f6f4 v[22:25], v[110:113], v[62:65], v[22:25] cbsz:4 blgp:4
	v_mfma_f32_16x16x128_f8f6f4 v[26:29], v[82:85], v[66:69], v[14:17] cbsz:4 blgp:4
	v_mfma_f32_16x16x128_f8f6f4 v[26:29], v[102:105], v[70:73], v[26:29] cbsz:4 blgp:4
	v_mfma_f32_16x16x128_f8f6f4 v[30:33], v[94:97], v[66:69], v[10:13] cbsz:4 blgp:4
	v_mfma_f32_16x16x128_f8f6f4 v[30:33], v[110:113], v[70:73], v[30:33] cbsz:4 blgp:4
	v_mfma_f32_16x16x128_f8f6f4 v[34:37], v[82:85], v[74:77], v[14:17] cbsz:4 blgp:4
	v_mfma_f32_16x16x128_f8f6f4 v[34:37], v[102:105], v[78:81], v[34:37] cbsz:4 blgp:4
	v_mfma_f32_16x16x128_f8f6f4 v[38:41], v[94:97], v[74:77], v[10:13] cbsz:4 blgp:4
	v_mfma_f32_16x16x128_f8f6f4 v[38:41], v[110:113], v[78:81], v[38:41] cbsz:4 blgp:4
	v_mfma_f32_16x16x128_f8f6f4 v[42:45], v[82:85], v[86:89], v[14:17] cbsz:4 blgp:4
	v_mfma_f32_16x16x128_f8f6f4 v[42:45], v[102:105], v[90:93], v[42:45] cbsz:4 blgp:4
	v_mfma_f32_16x16x128_f8f6f4 v[46:49], v[94:97], v[86:89], v[10:13] cbsz:4 blgp:4
	v_mfma_f32_16x16x128_f8f6f4 v[46:49], v[110:113], v[90:93], v[46:49] cbsz:4 blgp:4
	v_mfma_f32_16x16x128_f8f6f4 v[50:53], v[142:145], v[58:61], v[6:9] cbsz:4 blgp:4
	v_mfma_f32_16x16x128_f8f6f4 v[50:53], v[168:171], v[62:65], v[50:53] cbsz:4 blgp:4
	v_mfma_f32_16x16x128_f8f6f4 v[54:57], v[156:159], v[58:61], v[2:5] cbsz:4 blgp:4
	v_mfma_f32_16x16x128_f8f6f4 v[54:57], v[172:175], v[62:65], v[54:57] cbsz:4 blgp:4
	v_mfma_f32_16x16x128_f8f6f4 v[58:61], v[142:145], v[66:69], v[6:9] cbsz:4 blgp:4
	v_mfma_f32_16x16x128_f8f6f4 v[58:61], v[168:171], v[70:73], v[58:61] cbsz:4 blgp:4
	v_mfma_f32_16x16x128_f8f6f4 v[62:65], v[156:159], v[66:69], v[2:5] cbsz:4 blgp:4
	v_mfma_f32_16x16x128_f8f6f4 v[62:65], v[172:175], v[70:73], v[62:65] cbsz:4 blgp:4
	v_mfma_f32_16x16x128_f8f6f4 v[66:69], v[142:145], v[74:77], v[6:9] cbsz:4 blgp:4
	v_mfma_f32_16x16x128_f8f6f4 v[66:69], v[168:171], v[78:81], v[66:69] cbsz:4 blgp:4
	v_mfma_f32_16x16x128_f8f6f4 v[70:73], v[156:159], v[74:77], v[2:5] cbsz:4 blgp:4
	v_mfma_f32_16x16x128_f8f6f4 v[70:73], v[172:175], v[78:81], v[70:73] cbsz:4 blgp:4
	v_mfma_f32_16x16x128_f8f6f4 v[74:77], v[142:145], v[86:89], v[6:9] cbsz:4 blgp:4
	v_mfma_f32_16x16x128_f8f6f4 v[74:77], v[168:171], v[90:93], v[74:77] cbsz:4 blgp:4
	v_mfma_f32_16x16x128_f8f6f4 v[78:81], v[156:159], v[86:89], v[2:5] cbsz:4 blgp:4
	v_mfma_f32_16x16x128_f8f6f4 v[78:81], v[172:175], v[90:93], v[78:81] cbsz:4 blgp:4
	s_setprio 0
	s_barrier
	s_mov_b32 m0, s56
	s_nop 0
	global_load_lds_dwordx4 v148, s[50:51] sc1
	s_mov_b32 m0, s57
	s_nop 0
	global_load_lds_dwordx4 v152, s[50:51] sc1
	ds_read_b128 v[114:117], v165 offset:16384
	ds_read_b128 v[122:125], v165 offset:18432
	ds_read_b128 v[130:133], v166 offset:16384
	ds_read_b128 v[134:137], v166 offset:18432
	ds_read_b128 v[176:179], v165 offset:20480
	ds_read_b128 v[180:183], v165 offset:22528
	ds_read_b128 v[184:187], v166 offset:20480
	ds_read_b128 v[188:191], v166 offset:22528
	s_mov_b32 m0, s55
	s_nop 0
	global_load_lds_dwordx4 v146, s[48:49] sc1
	s_mov_b32 m0, s58
	s_nop 0
	global_load_lds_dwordx4 v150, s[48:49] sc1
	s_add_u32 s50, s50, s24
	s_addc_u32 s51, s51, s25
	s_mov_b32 m0, s59
	s_nop 0
	global_load_lds_dwordx4 v148, s[50:51] sc1
	s_mov_b32 m0, s60
	s_nop 0
	global_load_lds_dwordx4 v152, s[50:51] sc1
	s_waitcnt vmcnt(8)
	s_waitcnt lgkmcnt(0)
	s_barrier
	s_setprio 1
	v_mfma_f32_16x16x128_f8f6f4 v[86:89], v[82:85], v[114:117], v[14:17] cbsz:4 blgp:4
	v_mfma_f32_16x16x128_f8f6f4 v[86:89], v[102:105], v[130:133], v[86:89] cbsz:4 blgp:4
	v_mfma_f32_16x16x128_f8f6f4 v[90:93], v[94:97], v[114:117], v[10:13] cbsz:4 blgp:4
	v_mfma_f32_16x16x128_f8f6f4 v[90:93], v[110:113], v[130:133], v[90:93] cbsz:4 blgp:4
	v_mfma_f32_16x16x128_f8f6f4 v[98:101], v[82:85], v[122:125], v[14:17] cbsz:4 blgp:4
	v_mfma_f32_16x16x128_f8f6f4 v[98:101], v[102:105], v[134:137], v[98:101] cbsz:4 blgp:4
	v_mfma_f32_16x16x128_f8f6f4 v[106:109], v[94:97], v[122:125], v[10:13] cbsz:4 blgp:4
	v_mfma_f32_16x16x128_f8f6f4 v[106:109], v[110:113], v[134:137], v[106:109] cbsz:4 blgp:4
	v_mfma_f32_16x16x128_f8f6f4 v[118:121], v[82:85], v[176:179], v[14:17] cbsz:4 blgp:4
	v_mfma_f32_16x16x128_f8f6f4 v[118:121], v[102:105], v[184:187], v[118:121] cbsz:4 blgp:4
	v_mfma_f32_16x16x128_f8f6f4 v[126:129], v[94:97], v[176:179], v[10:13] cbsz:4 blgp:4
	v_mfma_f32_16x16x128_f8f6f4 v[126:129], v[110:113], v[184:187], v[126:129] cbsz:4 blgp:4
	v_mfma_f32_16x16x128_f8f6f4 v[138:141], v[82:85], v[180:183], v[14:17] cbsz:4 blgp:4
	v_mfma_f32_16x16x128_f8f6f4 v[138:141], v[102:105], v[188:191], v[138:141] cbsz:4 blgp:4
	v_mfma_f32_16x16x128_f8f6f4 v[82:85], v[94:97], v[180:183], v[10:13] cbsz:4 blgp:4
	v_mfma_f32_16x16x128_f8f6f4 v[82:85], v[110:113], v[188:191], v[82:85] cbsz:4 blgp:4
	v_mfma_f32_16x16x128_f8f6f4 v[94:97], v[142:145], v[114:117], v[6:9] cbsz:4 blgp:4
	v_mfma_f32_16x16x128_f8f6f4 v[94:97], v[168:171], v[130:133], v[94:97] cbsz:4 blgp:4
	v_mfma_f32_16x16x128_f8f6f4 v[102:105], v[156:159], v[114:117], v[2:5] cbsz:4 blgp:4
	v_mfma_f32_16x16x128_f8f6f4 v[102:105], v[172:175], v[130:133], v[102:105] cbsz:4 blgp:4
	v_mfma_f32_16x16x128_f8f6f4 v[110:113], v[142:145], v[122:125], v[6:9] cbsz:4 blgp:4
	v_mfma_f32_16x16x128_f8f6f4 v[110:113], v[168:171], v[134:137], v[110:113] cbsz:4 blgp:4
	v_mfma_f32_16x16x128_f8f6f4 v[114:117], v[156:159], v[122:125], v[2:5] cbsz:4 blgp:4
	v_mfma_f32_16x16x128_f8f6f4 v[114:117], v[172:175], v[134:137], v[114:117] cbsz:4 blgp:4
	v_mfma_f32_16x16x128_f8f6f4 v[122:125], v[142:145], v[176:179], v[6:9] cbsz:4 blgp:4
	v_mfma_f32_16x16x128_f8f6f4 v[122:125], v[168:171], v[184:187], v[122:125] cbsz:4 blgp:4
	v_mfma_f32_16x16x128_f8f6f4 v[130:133], v[156:159], v[176:179], v[2:5] cbsz:4 blgp:4
	v_mfma_f32_16x16x128_f8f6f4 v[130:133], v[172:175], v[184:187], v[130:133] cbsz:4 blgp:4
	v_mfma_f32_16x16x128_f8f6f4 v[134:137], v[142:145], v[180:183], v[6:9] cbsz:4 blgp:4
	v_mfma_f32_16x16x128_f8f6f4 v[134:137], v[168:171], v[188:191], v[134:137] cbsz:4 blgp:4
	v_mfma_f32_16x16x128_f8f6f4 v[142:145], v[156:159], v[180:183], v[2:5] cbsz:4 blgp:4
	v_mfma_f32_16x16x128_f8f6f4 v[142:145], v[172:175], v[188:191], v[142:145] cbsz:4 blgp:4
	s_setprio 0
	s_barrier
	ds_read_b128 v[156:159], v163 offset:32768
	ds_read_b128 v[168:171], v163 offset:34816
	ds_read_b128 v[172:175], v164 offset:32768
	ds_read_b128 v[176:179], v164 offset:34816
	ds_read_b128 v[180:183], v165 offset:32768
	ds_read_b128 v[184:187], v165 offset:34816
	ds_read_b128 v[188:191], v166 offset:32768
	ds_read_b128 v[192:195], v166 offset:34816
	ds_read_b128 v[196:199], v165 offset:36864
	ds_read_b128 v[200:203], v165 offset:38912
	ds_read_b128 v[204:207], v166 offset:36864
	ds_read_b128 v[208:211], v166 offset:38912
	s_add_u32 s48, s48, s22
	s_addc_u32 s49, s49, s23
	s_mov_b32 m0, s61
	s_nop 0
	global_load_lds_dwordx4 v146, s[48:49] sc1
	s_mov_b32 m0, s62
	s_nop 0
	global_load_lds_dwordx4 v150, s[48:49] sc1
	s_waitcnt lgkmcnt(8)
	ds_read_b128 v[212:215], v163 offset:49152
	ds_read_b128 v[216:219], v163 offset:51200
	ds_read_b128 v[220:223], v164 offset:49152
	ds_read_b128 v[224:227], v164 offset:51200
	s_waitcnt vmcnt(8)
	s_waitcnt lgkmcnt(0)
	s_barrier
	s_waitcnt lgkmcnt(0)
	s_setprio 1
	v_mfma_f32_16x16x128_f8f6f4 v[18:21], v[156:159], v[180:183], v[18:21] cbsz:4 blgp:4
	v_mfma_f32_16x16x128_f8f6f4 v[18:21], v[172:175], v[188:191], v[18:21] cbsz:4 blgp:4
	v_mfma_f32_16x16x128_f8f6f4 v[22:25], v[168:171], v[180:183], v[22:25] cbsz:4 blgp:4
	v_mfma_f32_16x16x128_f8f6f4 v[22:25], v[176:179], v[188:191], v[22:25] cbsz:4 blgp:4
	v_mfma_f32_16x16x128_f8f6f4 v[26:29], v[156:159], v[184:187], v[26:29] cbsz:4 blgp:4
	v_mfma_f32_16x16x128_f8f6f4 v[26:29], v[172:175], v[192:195], v[26:29] cbsz:4 blgp:4
	v_mfma_f32_16x16x128_f8f6f4 v[30:33], v[168:171], v[184:187], v[30:33] cbsz:4 blgp:4
	v_mfma_f32_16x16x128_f8f6f4 v[30:33], v[176:179], v[192:195], v[30:33] cbsz:4 blgp:4
	v_mfma_f32_16x16x128_f8f6f4 v[34:37], v[156:159], v[196:199], v[34:37] cbsz:4 blgp:4
	v_mfma_f32_16x16x128_f8f6f4 v[34:37], v[172:175], v[204:207], v[34:37] cbsz:4 blgp:4
	v_mfma_f32_16x16x128_f8f6f4 v[38:41], v[168:171], v[196:199], v[38:41] cbsz:4 blgp:4
	v_mfma_f32_16x16x128_f8f6f4 v[38:41], v[176:179], v[204:207], v[38:41] cbsz:4 blgp:4
	v_mfma_f32_16x16x128_f8f6f4 v[42:45], v[156:159], v[200:203], v[42:45] cbsz:4 blgp:4
	v_mfma_f32_16x16x128_f8f6f4 v[42:45], v[172:175], v[208:211], v[42:45] cbsz:4 blgp:4
	v_mfma_f32_16x16x128_f8f6f4 v[46:49], v[168:171], v[200:203], v[46:49] cbsz:4 blgp:4
	v_mfma_f32_16x16x128_f8f6f4 v[46:49], v[176:179], v[208:211], v[46:49] cbsz:4 blgp:4
	v_mfma_f32_16x16x128_f8f6f4 v[50:53], v[212:215], v[180:183], v[50:53] cbsz:4 blgp:4
	v_mfma_f32_16x16x128_f8f6f4 v[50:53], v[220:223], v[188:191], v[50:53] cbsz:4 blgp:4
	v_mfma_f32_16x16x128_f8f6f4 v[54:57], v[216:219], v[180:183], v[54:57] cbsz:4 blgp:4
	v_mfma_f32_16x16x128_f8f6f4 v[54:57], v[224:227], v[188:191], v[54:57] cbsz:4 blgp:4
	v_mfma_f32_16x16x128_f8f6f4 v[58:61], v[212:215], v[184:187], v[58:61] cbsz:4 blgp:4
	v_mfma_f32_16x16x128_f8f6f4 v[58:61], v[220:223], v[192:195], v[58:61] cbsz:4 blgp:4
	v_mfma_f32_16x16x128_f8f6f4 v[62:65], v[216:219], v[184:187], v[62:65] cbsz:4 blgp:4
	v_mfma_f32_16x16x128_f8f6f4 v[62:65], v[224:227], v[192:195], v[62:65] cbsz:4 blgp:4
	v_mfma_f32_16x16x128_f8f6f4 v[66:69], v[212:215], v[196:199], v[66:69] cbsz:4 blgp:4
	v_mfma_f32_16x16x128_f8f6f4 v[66:69], v[220:223], v[204:207], v[66:69] cbsz:4 blgp:4
	v_mfma_f32_16x16x128_f8f6f4 v[70:73], v[216:219], v[196:199], v[70:73] cbsz:4 blgp:4
	v_mfma_f32_16x16x128_f8f6f4 v[70:73], v[224:227], v[204:207], v[70:73] cbsz:4 blgp:4
	v_mfma_f32_16x16x128_f8f6f4 v[74:77], v[212:215], v[200:203], v[74:77] cbsz:4 blgp:4
	v_mfma_f32_16x16x128_f8f6f4 v[74:77], v[220:223], v[208:211], v[74:77] cbsz:4 blgp:4
	v_mfma_f32_16x16x128_f8f6f4 v[78:81], v[216:219], v[200:203], v[78:81] cbsz:4 blgp:4
	v_mfma_f32_16x16x128_f8f6f4 v[78:81], v[224:227], v[208:211], v[78:81] cbsz:4 blgp:4
	s_setprio 0
	s_barrier
	s_mov_b32 m0, s65
	s_nop 0
	global_load_lds_dwordx4 v148, s[44:45] sc1
	s_mov_b32 m0, s66
	s_nop 0
	global_load_lds_dwordx4 v152, s[44:45] sc1
	ds_read_b128 v[180:183], v165 offset:49152
	ds_read_b128 v[184:187], v165 offset:51200
	ds_read_b128 v[188:191], v166 offset:49152
	ds_read_b128 v[192:195], v166 offset:51200
	ds_read_b128 v[196:199], v165 offset:53248
	ds_read_b128 v[200:203], v165 offset:55296
	ds_read_b128 v[204:207], v166 offset:53248
	ds_read_b128 v[208:211], v166 offset:55296
	s_mov_b32 m0, s67
	s_nop 0
	global_load_lds_dwordx4 v146, s[46:47] sc1
	s_mov_b32 m0, s68
	s_nop 0
	global_load_lds_dwordx4 v150, s[46:47] sc1
	s_add_u32 s44, s44, s24
	s_addc_u32 s45, s45, s25
	s_mov_b32 m0, s69
	s_nop 0
	global_load_lds_dwordx4 v148, s[44:45] sc1
	s_mov_b32 m0, s70
	s_nop 0
	global_load_lds_dwordx4 v152, s[44:45] sc1
	s_waitcnt vmcnt(8)
	s_waitcnt lgkmcnt(0)
	s_barrier
	s_setprio 1
	v_mfma_f32_16x16x128_f8f6f4 v[86:89], v[156:159], v[180:183], v[86:89] cbsz:4 blgp:4
	v_mfma_f32_16x16x128_f8f6f4 v[86:89], v[172:175], v[188:191], v[86:89] cbsz:4 blgp:4
	v_mfma_f32_16x16x128_f8f6f4 v[90:93], v[168:171], v[180:183], v[90:93] cbsz:4 blgp:4
	v_mfma_f32_16x16x128_f8f6f4 v[90:93], v[176:179], v[188:191], v[90:93] cbsz:4 blgp:4
	v_mfma_f32_16x16x128_f8f6f4 v[98:101], v[156:159], v[184:187], v[98:101] cbsz:4 blgp:4
	v_mfma_f32_16x16x128_f8f6f4 v[98:101], v[172:175], v[192:195], v[98:101] cbsz:4 blgp:4
	v_mfma_f32_16x16x128_f8f6f4 v[106:109], v[168:171], v[184:187], v[106:109] cbsz:4 blgp:4
	v_mfma_f32_16x16x128_f8f6f4 v[106:109], v[176:179], v[192:195], v[106:109] cbsz:4 blgp:4
	v_mfma_f32_16x16x128_f8f6f4 v[118:121], v[156:159], v[196:199], v[118:121] cbsz:4 blgp:4
	v_mfma_f32_16x16x128_f8f6f4 v[118:121], v[172:175], v[204:207], v[118:121] cbsz:4 blgp:4
	v_mfma_f32_16x16x128_f8f6f4 v[126:129], v[168:171], v[196:199], v[126:129] cbsz:4 blgp:4
	v_mfma_f32_16x16x128_f8f6f4 v[126:129], v[176:179], v[204:207], v[126:129] cbsz:4 blgp:4
	v_mfma_f32_16x16x128_f8f6f4 v[138:141], v[156:159], v[200:203], v[138:141] cbsz:4 blgp:4
	v_mfma_f32_16x16x128_f8f6f4 v[138:141], v[172:175], v[208:211], v[138:141] cbsz:4 blgp:4
	v_mfma_f32_16x16x128_f8f6f4 v[82:85], v[168:171], v[200:203], v[82:85] cbsz:4 blgp:4
	v_mfma_f32_16x16x128_f8f6f4 v[82:85], v[176:179], v[208:211], v[82:85] cbsz:4 blgp:4
	v_mfma_f32_16x16x128_f8f6f4 v[94:97], v[212:215], v[180:183], v[94:97] cbsz:4 blgp:4
	v_mfma_f32_16x16x128_f8f6f4 v[94:97], v[220:223], v[188:191], v[94:97] cbsz:4 blgp:4
	v_mfma_f32_16x16x128_f8f6f4 v[102:105], v[216:219], v[180:183], v[102:105] cbsz:4 blgp:4
	v_mfma_f32_16x16x128_f8f6f4 v[102:105], v[224:227], v[188:191], v[102:105] cbsz:4 blgp:4
	v_mfma_f32_16x16x128_f8f6f4 v[110:113], v[212:215], v[184:187], v[110:113] cbsz:4 blgp:4
	v_mfma_f32_16x16x128_f8f6f4 v[110:113], v[220:223], v[192:195], v[110:113] cbsz:4 blgp:4
	v_mfma_f32_16x16x128_f8f6f4 v[114:117], v[216:219], v[184:187], v[114:117] cbsz:4 blgp:4
	v_mfma_f32_16x16x128_f8f6f4 v[114:117], v[224:227], v[192:195], v[114:117] cbsz:4 blgp:4
	v_mfma_f32_16x16x128_f8f6f4 v[122:125], v[212:215], v[196:199], v[122:125] cbsz:4 blgp:4
	v_mfma_f32_16x16x128_f8f6f4 v[122:125], v[220:223], v[204:207], v[122:125] cbsz:4 blgp:4
	v_mfma_f32_16x16x128_f8f6f4 v[130:133], v[216:219], v[196:199], v[130:133] cbsz:4 blgp:4
	v_mfma_f32_16x16x128_f8f6f4 v[130:133], v[224:227], v[204:207], v[130:133] cbsz:4 blgp:4
	v_mfma_f32_16x16x128_f8f6f4 v[134:137], v[212:215], v[200:203], v[134:137] cbsz:4 blgp:4
	v_mfma_f32_16x16x128_f8f6f4 v[134:137], v[220:223], v[208:211], v[134:137] cbsz:4 blgp:4
	v_mfma_f32_16x16x128_f8f6f4 v[142:145], v[216:219], v[200:203], v[142:145] cbsz:4 blgp:4
	v_mfma_f32_16x16x128_f8f6f4 v[142:145], v[224:227], v[208:211], v[142:145] cbsz:4 blgp:4
	s_setprio 0
	s_andn2_b64 vcc, exec, s[34:35]
	s_barrier
	s_cbranch_vccnz .LBB5_4
	s_ashr_i32 s29, s28, 31
	s_lshl_b64 s[44:45], s[28:29], 10
	s_add_u32 s44, s10, s44
	s_addc_u32 s45, s11, s45
	s_add_u32 s29, s42, 0x200
	s_addc_u32 s79, s43, 0
	s_add_u32 s80, s40, 0x200
	s_addc_u32 s81, s41, 0
	s_add_u32 s40, s82, 0x180
	s_addc_u32 s41, s83, 0
	s_mov_b32 s82, 4
	s_cmp_eq_u32 s64, s82
	s_cselect_b64 s[42:43], -1, 0
	s_cmp_lg_u32 s64, s82
	s_cbranch_scc1 .LBB5_15

.LBB5_15:
	ds_read_b128 v[156:159], v163
	ds_read_b128 v[168:171], v163 offset:2048
	ds_read_b128 v[172:175], v164
	ds_read_b128 v[176:179], v164 offset:2048
	s_and_b64 s[42:43], s[42:43], exec
	s_cselect_b32 s48, s38, s29
	s_cselect_b32 s49, s39, s79
	s_cselect_b32 s51, s5, s81
	s_cselect_b32 s50, s4, s80
	s_add_u32 s46, s48, 0x80
	s_addc_u32 s47, s49, 0
	s_add_u32 s42, s50, 0x80
	s_addc_u32 s43, s51, 0
	ds_read_b128 v[180:183], v165
	ds_read_b128 v[184:187], v165 offset:2048
	ds_read_b128 v[188:191], v166
	ds_read_b128 v[192:195], v166 offset:2048
	ds_read_b128 v[196:199], v165 offset:4096
	ds_read_b128 v[200:203], v165 offset:6144
	ds_read_b128 v[204:207], v166 offset:4096
	ds_read_b128 v[208:211], v166 offset:6144
	s_mov_b32 m0, s71
	s_nop 0
	global_load_lds_dwordx4 v146, s[40:41] sc1
	s_mov_b32 m0, s72
	s_nop 0
	global_load_lds_dwordx4 v150, s[40:41] sc1
	s_waitcnt lgkmcnt(8)
	ds_read_b128 v[212:215], v163 offset:16384
	ds_read_b128 v[216:219], v163 offset:18432
	ds_read_b128 v[220:223], v164 offset:16384
	ds_read_b128 v[224:227], v164 offset:18432
	s_waitcnt vmcnt(8)
	s_waitcnt lgkmcnt(0)
	s_barrier
	s_waitcnt lgkmcnt(0)
	s_setprio 1
	v_mfma_f32_16x16x128_f8f6f4 v[18:21], v[156:159], v[180:183], v[18:21] cbsz:4 blgp:4
	v_mfma_f32_16x16x128_f8f6f4 v[18:21], v[172:175], v[188:191], v[18:21] cbsz:4 blgp:4
	v_mfma_f32_16x16x128_f8f6f4 v[22:25], v[168:171], v[180:183], v[22:25] cbsz:4 blgp:4
	v_mfma_f32_16x16x128_f8f6f4 v[22:25], v[176:179], v[188:191], v[22:25] cbsz:4 blgp:4
	v_mfma_f32_16x16x128_f8f6f4 v[26:29], v[156:159], v[184:187], v[26:29] cbsz:4 blgp:4
	v_mfma_f32_16x16x128_f8f6f4 v[26:29], v[172:175], v[192:195], v[26:29] cbsz:4 blgp:4
	v_mfma_f32_16x16x128_f8f6f4 v[30:33], v[168:171], v[184:187], v[30:33] cbsz:4 blgp:4
	v_mfma_f32_16x16x128_f8f6f4 v[30:33], v[176:179], v[192:195], v[30:33] cbsz:4 blgp:4
	v_mfma_f32_16x16x128_f8f6f4 v[34:37], v[156:159], v[196:199], v[34:37] cbsz:4 blgp:4
	v_mfma_f32_16x16x128_f8f6f4 v[34:37], v[172:175], v[204:207], v[34:37] cbsz:4 blgp:4
	v_mfma_f32_16x16x128_f8f6f4 v[38:41], v[168:171], v[196:199], v[38:41] cbsz:4 blgp:4
	v_mfma_f32_16x16x128_f8f6f4 v[38:41], v[176:179], v[204:207], v[38:41] cbsz:4 blgp:4
	v_mfma_f32_16x16x128_f8f6f4 v[42:45], v[156:159], v[200:203], v[42:45] cbsz:4 blgp:4
	v_mfma_f32_16x16x128_f8f6f4 v[42:45], v[172:175], v[208:211], v[42:45] cbsz:4 blgp:4
	v_mfma_f32_16x16x128_f8f6f4 v[46:49], v[168:171], v[200:203], v[46:49] cbsz:4 blgp:4
	v_mfma_f32_16x16x128_f8f6f4 v[46:49], v[176:179], v[208:211], v[46:49] cbsz:4 blgp:4
	v_mfma_f32_16x16x128_f8f6f4 v[50:53], v[212:215], v[180:183], v[50:53] cbsz:4 blgp:4
	v_mfma_f32_16x16x128_f8f6f4 v[50:53], v[220:223], v[188:191], v[50:53] cbsz:4 blgp:4
	v_mfma_f32_16x16x128_f8f6f4 v[54:57], v[216:219], v[180:183], v[54:57] cbsz:4 blgp:4
	v_mfma_f32_16x16x128_f8f6f4 v[54:57], v[224:227], v[188:191], v[54:57] cbsz:4 blgp:4
	v_mfma_f32_16x16x128_f8f6f4 v[58:61], v[212:215], v[184:187], v[58:61] cbsz:4 blgp:4
	v_mfma_f32_16x16x128_f8f6f4 v[58:61], v[220:223], v[192:195], v[58:61] cbsz:4 blgp:4
	v_mfma_f32_16x16x128_f8f6f4 v[62:65], v[216:219], v[184:187], v[62:65] cbsz:4 blgp:4
	v_mfma_f32_16x16x128_f8f6f4 v[62:65], v[224:227], v[192:195], v[62:65] cbsz:4 blgp:4
	v_mfma_f32_16x16x128_f8f6f4 v[66:69], v[212:215], v[196:199], v[66:69] cbsz:4 blgp:4
	v_mfma_f32_16x16x128_f8f6f4 v[66:69], v[220:223], v[204:207], v[66:69] cbsz:4 blgp:4
	v_mfma_f32_16x16x128_f8f6f4 v[70:73], v[216:219], v[196:199], v[70:73] cbsz:4 blgp:4
	v_mfma_f32_16x16x128_f8f6f4 v[70:73], v[224:227], v[204:207], v[70:73] cbsz:4 blgp:4
	v_mfma_f32_16x16x128_f8f6f4 v[74:77], v[212:215], v[200:203], v[74:77] cbsz:4 blgp:4
	v_mfma_f32_16x16x128_f8f6f4 v[74:77], v[220:223], v[208:211], v[74:77] cbsz:4 blgp:4
	v_mfma_f32_16x16x128_f8f6f4 v[78:81], v[216:219], v[200:203], v[78:81] cbsz:4 blgp:4
	v_mfma_f32_16x16x128_f8f6f4 v[78:81], v[224:227], v[208:211], v[78:81] cbsz:4 blgp:4
	s_setprio 0
	s_barrier
	s_mov_b32 m0, s56
	s_nop 0
	global_load_lds_dwordx4 v148, s[50:51] sc1
	s_mov_b32 m0, s57
	s_nop 0
	global_load_lds_dwordx4 v152, s[50:51] sc1
	ds_read_b128 v[180:183], v165 offset:16384
	ds_read_b128 v[184:187], v165 offset:18432
	ds_read_b128 v[188:191], v166 offset:16384
	ds_read_b128 v[192:195], v166 offset:18432
	ds_read_b128 v[196:199], v165 offset:20480
	ds_read_b128 v[200:203], v165 offset:22528
	ds_read_b128 v[204:207], v166 offset:20480
	ds_read_b128 v[208:211], v166 offset:22528
	s_mov_b32 m0, s55
	s_nop 0
	global_load_lds_dwordx4 v146, s[48:49] sc1
	s_mov_b32 m0, s58
	s_nop 0
	global_load_lds_dwordx4 v150, s[48:49] sc1
	s_add_u32 s50, s50, s24
	s_addc_u32 s51, s51, s25
	s_mov_b32 m0, s59
	s_nop 0
	global_load_lds_dwordx4 v148, s[50:51] sc1
	s_mov_b32 m0, s60
	s_nop 0
	global_load_lds_dwordx4 v152, s[50:51] sc1
	s_waitcnt vmcnt(8)
	s_waitcnt lgkmcnt(0)
	s_barrier
	s_setprio 1
	v_mfma_f32_16x16x128_f8f6f4 v[86:89], v[156:159], v[180:183], v[86:89] cbsz:4 blgp:4
	v_mfma_f32_16x16x128_f8f6f4 v[86:89], v[172:175], v[188:191], v[86:89] cbsz:4 blgp:4
	v_mfma_f32_16x16x128_f8f6f4 v[90:93], v[168:171], v[180:183], v[90:93] cbsz:4 blgp:4
	v_mfma_f32_16x16x128_f8f6f4 v[90:93], v[176:179], v[188:191], v[90:93] cbsz:4 blgp:4
	v_mfma_f32_16x16x128_f8f6f4 v[98:101], v[156:159], v[184:187], v[98:101] cbsz:4 blgp:4
	v_mfma_f32_16x16x128_f8f6f4 v[98:101], v[172:175], v[192:195], v[98:101] cbsz:4 blgp:4
	v_mfma_f32_16x16x128_f8f6f4 v[106:109], v[168:171], v[184:187], v[106:109] cbsz:4 blgp:4
	v_mfma_f32_16x16x128_f8f6f4 v[106:109], v[176:179], v[192:195], v[106:109] cbsz:4 blgp:4
	v_mfma_f32_16x16x128_f8f6f4 v[118:121], v[156:159], v[196:199], v[118:121] cbsz:4 blgp:4
	v_mfma_f32_16x16x128_f8f6f4 v[118:121], v[172:175], v[204:207], v[118:121] cbsz:4 blgp:4
	v_mfma_f32_16x16x128_f8f6f4 v[126:129], v[168:171], v[196:199], v[126:129] cbsz:4 blgp:4
	v_mfma_f32_16x16x128_f8f6f4 v[126:129], v[176:179], v[204:207], v[126:129] cbsz:4 blgp:4
	v_mfma_f32_16x16x128_f8f6f4 v[138:141], v[156:159], v[200:203], v[138:141] cbsz:4 blgp:4
	v_mfma_f32_16x16x128_f8f6f4 v[138:141], v[172:175], v[208:211], v[138:141] cbsz:4 blgp:4
	v_mfma_f32_16x16x128_f8f6f4 v[82:85], v[168:171], v[200:203], v[82:85] cbsz:4 blgp:4
	v_mfma_f32_16x16x128_f8f6f4 v[82:85], v[176:179], v[208:211], v[82:85] cbsz:4 blgp:4
	v_mfma_f32_16x16x128_f8f6f4 v[94:97], v[212:215], v[180:183], v[94:97] cbsz:4 blgp:4
	v_mfma_f32_16x16x128_f8f6f4 v[94:97], v[220:223], v[188:191], v[94:97] cbsz:4 blgp:4
	v_mfma_f32_16x16x128_f8f6f4 v[102:105], v[216:219], v[180:183], v[102:105] cbsz:4 blgp:4
	v_mfma_f32_16x16x128_f8f6f4 v[102:105], v[224:227], v[188:191], v[102:105] cbsz:4 blgp:4
	v_mfma_f32_16x16x128_f8f6f4 v[110:113], v[212:215], v[184:187], v[110:113] cbsz:4 blgp:4
	v_mfma_f32_16x16x128_f8f6f4 v[110:113], v[220:223], v[192:195], v[110:113] cbsz:4 blgp:4
	v_mfma_f32_16x16x128_f8f6f4 v[114:117], v[216:219], v[184:187], v[114:117] cbsz:4 blgp:4
	v_mfma_f32_16x16x128_f8f6f4 v[114:117], v[224:227], v[192:195], v[114:117] cbsz:4 blgp:4
	v_mfma_f32_16x16x128_f8f6f4 v[122:125], v[212:215], v[196:199], v[122:125] cbsz:4 blgp:4
	v_mfma_f32_16x16x128_f8f6f4 v[122:125], v[220:223], v[204:207], v[122:125] cbsz:4 blgp:4
	v_mfma_f32_16x16x128_f8f6f4 v[130:133], v[216:219], v[196:199], v[130:133] cbsz:4 blgp:4
	v_mfma_f32_16x16x128_f8f6f4 v[130:133], v[224:227], v[204:207], v[130:133] cbsz:4 blgp:4
	v_mfma_f32_16x16x128_f8f6f4 v[134:137], v[212:215], v[200:203], v[134:137] cbsz:4 blgp:4
	v_mfma_f32_16x16x128_f8f6f4 v[134:137], v[220:223], v[208:211], v[134:137] cbsz:4 blgp:4
	v_mfma_f32_16x16x128_f8f6f4 v[142:145], v[216:219], v[200:203], v[142:145] cbsz:4 blgp:4
	v_mfma_f32_16x16x128_f8f6f4 v[142:145], v[224:227], v[208:211], v[142:145] cbsz:4 blgp:4
	s_setprio 0
	s_barrier
	ds_read_b128 v[156:159], v163 offset:32768
	ds_read_b128 v[168:171], v163 offset:34816
	ds_read_b128 v[172:175], v164 offset:32768
	ds_read_b128 v[176:179], v164 offset:34816
	ds_read_b128 v[180:183], v165 offset:32768
	ds_read_b128 v[184:187], v165 offset:34816
	ds_read_b128 v[188:191], v166 offset:32768
	ds_read_b128 v[192:195], v166 offset:34816
	ds_read_b128 v[196:199], v165 offset:36864
	ds_read_b128 v[200:203], v165 offset:38912
	ds_read_b128 v[204:207], v166 offset:36864
	ds_read_b128 v[208:211], v166 offset:38912
	s_add_u32 s48, s48, s22
	s_addc_u32 s49, s49, s23
	s_mov_b32 m0, s61
	s_nop 0
	global_load_lds_dwordx4 v146, s[48:49] sc1
	s_mov_b32 m0, s62
	s_nop 0
	global_load_lds_dwordx4 v150, s[48:49] sc1
	s_waitcnt lgkmcnt(8)
	ds_read_b128 v[212:215], v163 offset:49152
	ds_read_b128 v[216:219], v163 offset:51200
	ds_read_b128 v[220:223], v164 offset:49152
	ds_read_b128 v[224:227], v164 offset:51200
	s_waitcnt vmcnt(8)
	s_waitcnt lgkmcnt(0)
	s_barrier
	s_waitcnt lgkmcnt(0)
	s_setprio 1
	v_mfma_f32_16x16x128_f8f6f4 v[18:21], v[156:159], v[180:183], v[18:21] cbsz:4 blgp:4
	v_mfma_f32_16x16x128_f8f6f4 v[18:21], v[172:175], v[188:191], v[18:21] cbsz:4 blgp:4
	v_mfma_f32_16x16x128_f8f6f4 v[22:25], v[168:171], v[180:183], v[22:25] cbsz:4 blgp:4
	v_mfma_f32_16x16x128_f8f6f4 v[22:25], v[176:179], v[188:191], v[22:25] cbsz:4 blgp:4
	v_mfma_f32_16x16x128_f8f6f4 v[26:29], v[156:159], v[184:187], v[26:29] cbsz:4 blgp:4
	v_mfma_f32_16x16x128_f8f6f4 v[26:29], v[172:175], v[192:195], v[26:29] cbsz:4 blgp:4
	v_mfma_f32_16x16x128_f8f6f4 v[30:33], v[168:171], v[184:187], v[30:33] cbsz:4 blgp:4
	v_mfma_f32_16x16x128_f8f6f4 v[30:33], v[176:179], v[192:195], v[30:33] cbsz:4 blgp:4
	v_mfma_f32_16x16x128_f8f6f4 v[34:37], v[156:159], v[196:199], v[34:37] cbsz:4 blgp:4
	v_mfma_f32_16x16x128_f8f6f4 v[34:37], v[172:175], v[204:207], v[34:37] cbsz:4 blgp:4
	v_mfma_f32_16x16x128_f8f6f4 v[38:41], v[168:171], v[196:199], v[38:41] cbsz:4 blgp:4
	v_mfma_f32_16x16x128_f8f6f4 v[38:41], v[176:179], v[204:207], v[38:41] cbsz:4 blgp:4
	v_mfma_f32_16x16x128_f8f6f4 v[42:45], v[156:159], v[200:203], v[42:45] cbsz:4 blgp:4
	v_mfma_f32_16x16x128_f8f6f4 v[42:45], v[172:175], v[208:211], v[42:45] cbsz:4 blgp:4
	v_mfma_f32_16x16x128_f8f6f4 v[46:49], v[168:171], v[200:203], v[46:49] cbsz:4 blgp:4
	v_mfma_f32_16x16x128_f8f6f4 v[46:49], v[176:179], v[208:211], v[46:49] cbsz:4 blgp:4
	v_mfma_f32_16x16x128_f8f6f4 v[50:53], v[212:215], v[180:183], v[50:53] cbsz:4 blgp:4
	v_mfma_f32_16x16x128_f8f6f4 v[50:53], v[220:223], v[188:191], v[50:53] cbsz:4 blgp:4
	v_mfma_f32_16x16x128_f8f6f4 v[54:57], v[216:219], v[180:183], v[54:57] cbsz:4 blgp:4
	v_mfma_f32_16x16x128_f8f6f4 v[54:57], v[224:227], v[188:191], v[54:57] cbsz:4 blgp:4
	v_mfma_f32_16x16x128_f8f6f4 v[58:61], v[212:215], v[184:187], v[58:61] cbsz:4 blgp:4
	v_mfma_f32_16x16x128_f8f6f4 v[58:61], v[220:223], v[192:195], v[58:61] cbsz:4 blgp:4
	v_mfma_f32_16x16x128_f8f6f4 v[62:65], v[216:219], v[184:187], v[62:65] cbsz:4 blgp:4
	v_mfma_f32_16x16x128_f8f6f4 v[62:65], v[224:227], v[192:195], v[62:65] cbsz:4 blgp:4
	v_mfma_f32_16x16x128_f8f6f4 v[66:69], v[212:215], v[196:199], v[66:69] cbsz:4 blgp:4
	v_mfma_f32_16x16x128_f8f6f4 v[66:69], v[220:223], v[204:207], v[66:69] cbsz:4 blgp:4
	v_mfma_f32_16x16x128_f8f6f4 v[70:73], v[216:219], v[196:199], v[70:73] cbsz:4 blgp:4
	v_mfma_f32_16x16x128_f8f6f4 v[70:73], v[224:227], v[204:207], v[70:73] cbsz:4 blgp:4
	v_mfma_f32_16x16x128_f8f6f4 v[74:77], v[212:215], v[200:203], v[74:77] cbsz:4 blgp:4
	v_mfma_f32_16x16x128_f8f6f4 v[74:77], v[220:223], v[208:211], v[74:77] cbsz:4 blgp:4
	v_mfma_f32_16x16x128_f8f6f4 v[78:81], v[216:219], v[200:203], v[78:81] cbsz:4 blgp:4
	v_mfma_f32_16x16x128_f8f6f4 v[78:81], v[224:227], v[208:211], v[78:81] cbsz:4 blgp:4
	s_setprio 0
	s_barrier
	s_mov_b32 m0, s65
	s_nop 0
	global_load_lds_dwordx4 v148, s[42:43] sc1
	s_mov_b32 m0, s66
	s_nop 0
	global_load_lds_dwordx4 v152, s[42:43] sc1
	ds_read_b128 v[180:183], v165 offset:49152
	ds_read_b128 v[184:187], v165 offset:51200
	ds_read_b128 v[188:191], v166 offset:49152
	ds_read_b128 v[192:195], v166 offset:51200
	ds_read_b128 v[196:199], v165 offset:53248
	ds_read_b128 v[200:203], v165 offset:55296
	ds_read_b128 v[204:207], v166 offset:53248
	ds_read_b128 v[208:211], v166 offset:55296
	s_mov_b32 m0, s67
	s_nop 0
	global_load_lds_dwordx4 v146, s[46:47] sc1
	s_mov_b32 m0, s68
	s_nop 0
	global_load_lds_dwordx4 v150, s[46:47] sc1
	s_add_u32 s42, s42, s24
	s_addc_u32 s43, s43, s25
	s_mov_b32 m0, s69
	s_nop 0
	global_load_lds_dwordx4 v148, s[42:43] sc1
	s_mov_b32 m0, s70
	s_nop 0
	global_load_lds_dwordx4 v152, s[42:43] sc1
	s_waitcnt vmcnt(8)
	s_waitcnt lgkmcnt(0)
	s_barrier
	s_setprio 1
	v_mfma_f32_16x16x128_f8f6f4 v[86:89], v[156:159], v[180:183], v[86:89] cbsz:4 blgp:4
	v_mfma_f32_16x16x128_f8f6f4 v[86:89], v[172:175], v[188:191], v[86:89] cbsz:4 blgp:4
	v_mfma_f32_16x16x128_f8f6f4 v[90:93], v[168:171], v[180:183], v[90:93] cbsz:4 blgp:4
	v_mfma_f32_16x16x128_f8f6f4 v[90:93], v[176:179], v[188:191], v[90:93] cbsz:4 blgp:4
	v_mfma_f32_16x16x128_f8f6f4 v[98:101], v[156:159], v[184:187], v[98:101] cbsz:4 blgp:4
	v_mfma_f32_16x16x128_f8f6f4 v[98:101], v[172:175], v[192:195], v[98:101] cbsz:4 blgp:4
	v_mfma_f32_16x16x128_f8f6f4 v[106:109], v[168:171], v[184:187], v[106:109] cbsz:4 blgp:4
	v_mfma_f32_16x16x128_f8f6f4 v[106:109], v[176:179], v[192:195], v[106:109] cbsz:4 blgp:4
	v_mfma_f32_16x16x128_f8f6f4 v[118:121], v[156:159], v[196:199], v[118:121] cbsz:4 blgp:4
	v_mfma_f32_16x16x128_f8f6f4 v[118:121], v[172:175], v[204:207], v[118:121] cbsz:4 blgp:4
	v_mfma_f32_16x16x128_f8f6f4 v[126:129], v[168:171], v[196:199], v[126:129] cbsz:4 blgp:4
	v_mfma_f32_16x16x128_f8f6f4 v[126:129], v[176:179], v[204:207], v[126:129] cbsz:4 blgp:4
	v_mfma_f32_16x16x128_f8f6f4 v[138:141], v[156:159], v[200:203], v[138:141] cbsz:4 blgp:4
	v_mfma_f32_16x16x128_f8f6f4 v[138:141], v[172:175], v[208:211], v[138:141] cbsz:4 blgp:4
	v_mfma_f32_16x16x128_f8f6f4 v[82:85], v[168:171], v[200:203], v[82:85] cbsz:4 blgp:4
	v_mfma_f32_16x16x128_f8f6f4 v[82:85], v[176:179], v[208:211], v[82:85] cbsz:4 blgp:4
	v_mfma_f32_16x16x128_f8f6f4 v[94:97], v[212:215], v[180:183], v[94:97] cbsz:4 blgp:4
	v_mfma_f32_16x16x128_f8f6f4 v[94:97], v[220:223], v[188:191], v[94:97] cbsz:4 blgp:4
	v_mfma_f32_16x16x128_f8f6f4 v[102:105], v[216:219], v[180:183], v[102:105] cbsz:4 blgp:4
	v_mfma_f32_16x16x128_f8f6f4 v[102:105], v[224:227], v[188:191], v[102:105] cbsz:4 blgp:4
	v_mfma_f32_16x16x128_f8f6f4 v[110:113], v[212:215], v[184:187], v[110:113] cbsz:4 blgp:4
	v_mfma_f32_16x16x128_f8f6f4 v[110:113], v[220:223], v[192:195], v[110:113] cbsz:4 blgp:4
	v_mfma_f32_16x16x128_f8f6f4 v[114:117], v[216:219], v[184:187], v[114:117] cbsz:4 blgp:4
	v_mfma_f32_16x16x128_f8f6f4 v[114:117], v[224:227], v[192:195], v[114:117] cbsz:4 blgp:4
	v_mfma_f32_16x16x128_f8f6f4 v[122:125], v[212:215], v[196:199], v[122:125] cbsz:4 blgp:4
	v_mfma_f32_16x16x128_f8f6f4 v[122:125], v[220:223], v[204:207], v[122:125] cbsz:4 blgp:4
	v_mfma_f32_16x16x128_f8f6f4 v[130:133], v[216:219], v[196:199], v[130:133] cbsz:4 blgp:4
	v_mfma_f32_16x16x128_f8f6f4 v[130:133], v[224:227], v[204:207], v[130:133] cbsz:4 blgp:4
	v_mfma_f32_16x16x128_f8f6f4 v[134:137], v[212:215], v[200:203], v[134:137] cbsz:4 blgp:4
	v_mfma_f32_16x16x128_f8f6f4 v[134:137], v[220:223], v[208:211], v[134:137] cbsz:4 blgp:4
	v_mfma_f32_16x16x128_f8f6f4 v[142:145], v[216:219], v[200:203], v[142:145] cbsz:4 blgp:4
	v_mfma_f32_16x16x128_f8f6f4 v[142:145], v[224:227], v[208:211], v[142:145] cbsz:4 blgp:4
	s_setprio 0
	s_add_i32 s42, s82, 2
	s_add_u32 s29, s29, 0x100
	s_addc_u32 s79, s79, 0
	s_add_u32 s80, s80, 0x100
	s_addc_u32 s81, s81, 0
	s_add_u32 s40, s40, 0x100
	s_addc_u32 s41, s41, 0
	s_cmp_ge_i32 s82, s64
	s_barrier
	s_cbranch_scc1 .LBB5_4
	s_mov_b32 s82, s42
	s_cmp_eq_u32 s64, s82
	s_cselect_b64 s[42:43], -1, 0
	s_cmp_lg_u32 s64, s82
	s_cbranch_scc0 .LBB5_14
	s_branch .LBB5_15

.LBB6_4:
	v_lshrrev_b32_e32 v5, 5, v0
	s_load_dwordx4 s[12:15], s[0:1], 0x18
	s_load_dwordx2 s[28:29], s[0:1], 0x28
	s_load_dwordx4 s[16:19], s[0:1], 0x0
	s_load_dword s6, s[0:1], 0x10
	s_load_dword s50, s[0:1], 0x30
	s_load_dword s51, s[0:1], 0x48
	v_lshlrev_b32_e32 v3, 4, v0
	v_and_b32_e32 v5, 4, v5
	v_lshrrev_b32_e32 v6, 3, v0
	v_lshrrev_b32_e32 v7, 2, v0
	v_lshrrev_b32_e32 v19, 1, v0
	v_lshlrev_b32_e32 v9, 1, v0
	v_and_b32_e32 v2, 16, v0
	v_and_b32_e32 v4, 0x70, v3
	v_and_b32_e32 v7, 64, v7
	v_and_or_b32 v5, v6, 3, v5
	v_and_b32_e32 v8, 48, v19
	v_and_b32_e32 v9, 64, v9
	v_or3_b32 v7, v8, v7, v5
	v_bitop3_b32 v2, v9, v4, v2 bitop3:0x36
	s_waitcnt lgkmcnt(0)
	v_mad_u64_u32 v[162:163], s[0:1], s6, v6, v[2:3]
	v_mad_u64_u32 v[164:165], s[0:1], s6, v7, v[2:3]
	v_or_b32_e32 v3, 0x2000, v3
	v_lshrrev_b32_e32 v4, 7, v3
	v_lshrrev_b32_e32 v3, 6, v3
	v_and_b32_e32 v3, 0xc0, v3
	v_or3_b32 v3, v8, v3, v5
	s_lshr_b32 s31, s49, 6
	v_mad_u64_u32 v[166:167], s[0:1], s6, v4, v[2:3]
	v_mad_u64_u32 v[168:169], s[0:1], s6, v3, v[2:3]
	s_ashr_i32 s7, s6, 31
	s_lshl_b32 s0, s31, 10
	s_lshl_b64 s[24:25], s[6:7], 8
	s_add_i32 s53, s0, 0
	s_lshr_b64 s[0:1], s[6:7], 24
	s_mul_i32 s1, s26, s0
	s_mul_hi_u32 s31, s26, s24
	s_add_i32 s1, s31, s1
	s_mul_i32 s27, s27, s24
	s_ashr_i32 s31, s30, 31
	s_add_i32 s27, s1, s27
	s_mul_i32 s36, s26, s24
	s_mul_i32 s1, s24, s31
	s_mul_hi_u32 s26, s24, s30
	s_add_i32 s1, s26, s1
	s_mul_i32 s0, s0, s30
	s_bfe_u32 s8, s49, 0x20006
	s_lshr_b32 s38, s49, 8
	s_lshl_b64 s[20:21], s[6:7], 7
	s_lshl_b64 s[22:23], s[6:7], 3
	s_add_i32 s1, s1, s0
	s_mul_i32 s0, s24, s30
	s_add_u32 s34, s18, s0
	v_bfe_u32 v1, v0, 4, 2
	s_addc_u32 s35, s19, s1
	s_lshl_b64 s[0:1], s[30:31], 10
	v_lshlrev_b32_e32 v18, 6, v1
	s_add_u32 s0, s14, s0
	v_lshl_or_b32 v163, s8, 8, v18
	s_addc_u32 s1, s15, s1
	global_load_dwordx4 v[14:17], v163, s[0:1]
	global_load_dwordx4 v[10:13], v163, s[0:1] offset:16
	global_load_dwordx4 v[6:9], v163, s[0:1] offset:32
	global_load_dwordx4 v[2:5], v163, s[0:1] offset:48
	s_add_i32 s54, s53, 0x10000
	s_mov_b32 m0, s54
	s_nop 0
	global_load_lds_dwordx4 v164, s[34:35] sc1
	s_add_i32 s55, s53, 0x12000
	s_mov_b32 m0, s55
	s_nop 0
	global_load_lds_dwordx4 v168, s[34:35] sc1
	s_add_u32 s36, s16, s36
	s_addc_u32 s37, s17, s27
	s_mov_b32 m0, s53
	s_nop 0
	global_load_lds_dwordx4 v162, s[36:37] sc1
	s_add_i32 s56, s53, 0x2000
	s_add_i32 s57, s53, 0x14000
	s_mov_b32 m0, s56
	s_nop 0
	global_load_lds_dwordx4 v166, s[36:37] sc1
	s_add_u32 s0, s34, s22
	s_addc_u32 s1, s35, s23
	s_mov_b32 m0, s57
	s_nop 0
	global_load_lds_dwordx4 v164, s[0:1] sc1
	s_add_i32 s58, s53, 0x16000
	s_add_i32 s59, s53, 0x4000
	s_mov_b32 m0, s58
	s_nop 0
	global_load_lds_dwordx4 v168, s[0:1] sc1
	s_add_u32 s40, s36, s20
	s_addc_u32 s41, s37, s21
	s_mov_b32 m0, s59
	s_nop 0
	global_load_lds_dwordx4 v162, s[40:41] sc1
	s_add_i32 s60, s53, 0x6000
	s_mov_b32 m0, s60
	s_nop 0
	global_load_lds_dwordx4 v166, s[40:41] sc1
	s_mov_b32 s52, 0
	s_mov_b32 s26, 0x10000
	s_cmp_lg_u32 s38, 1
	s_cbranch_scc1 .LBB6_6
	s_barrier
.LBB6_6:
	v_and_b32_e32 v20, 15, v0
	v_and_b32_e32 v0, 4, v0
	v_lshl_or_b32 v165, s38, 6, v20
	v_lshlrev_b32_e32 v21, 5, v1
	v_and_or_b32 v0, v19, 1, v0
	s_lshr_b32 s7, s7, 25
	v_lshlrev_b32_e32 v22, 7, v165
	v_lshlrev_b32_e32 v0, 4, v0
	v_or_b32_e32 v24, 16, v21
	s_add_i32 s7, s6, s7
	v_xor_b32_e32 v19, v0, v21
	v_bitop3_b32 v23, v22, v0, v21 bitop3:0xf6
	v_bitop3_b32 v21, v0, v21, 16 bitop3:0x1e
	v_bitop3_b32 v22, v22, v0, v24 bitop3:0xf6
	v_lshlrev_b32_e32 v0, 7, v20
	s_ashr_i32 s61, s7, 7
	v_lshl_or_b32 v0, s8, 12, v0
	s_add_i32 s62, s53, 0x18000
	v_or3_b32 v20, v19, v0, s26
	v_or3_b32 v21, v21, v0, s26
	s_add_u32 s26, s34, 0x80
	s_waitcnt vmcnt(0)
	s_barrier
	s_addc_u32 s27, s35, 0
	s_mov_b32 m0, s62
	s_nop 0
	global_load_lds_dwordx4 v164, s[26:27] sc1
	s_add_i32 s63, s53, 0x1a000
	s_add_i32 s64, s53, 0x8000
	s_mov_b32 m0, s63
	s_nop 0
	global_load_lds_dwordx4 v168, s[26:27] sc1
	s_add_u32 s26, s36, 0x80
	s_addc_u32 s27, s37, 0
	s_add_i32 s65, s53, 0xa000
	s_add_i32 s66, s53, 0x1c000
	s_add_u32 s0, s0, 0x80
	s_addc_u32 s1, s1, 0
	s_add_i32 s67, s53, 0x1e000
	s_mov_b32 m0, s64
	s_nop 0
	global_load_lds_dwordx4 v162, s[26:27] sc1
	s_cmpk_gt_i32 s6, 0x7f
	s_mov_b32 m0, s65
	s_nop 0
	global_load_lds_dwordx4 v166, s[26:27] sc1
	s_cselect_b64 s[26:27], -1, 0
	s_add_i32 s68, s53, 0xc000
	s_add_i32 s69, s53, 0xe000
	s_ashr_i32 s70, s51, 31
	s_ashr_i32 s71, s2, 31
	s_lshl_b32 s7, s8, 8
	s_add_u32 s28, s28, s7
	s_addc_u32 s29, s29, 0
	s_lshl_b32 s7, s8, 2
	s_mov_b32 m0, s66
	s_nop 0
	global_load_lds_dwordx4 v164, s[0:1] sc1
	v_mov_b32_e32 v19, 0
	s_add_u32 s72, s12, s7
	s_mov_b32 m0, s67
	s_nop 0
	global_load_lds_dwordx4 v168, s[0:1] sc1
	v_cmp_eq_u32_e64 s[0:1], 0, v1
	v_lshl_add_u64 v[0:1], s[28:29], 0, v[18:19]
	s_addc_u32 s73, s13, 0
	v_div_scale_f32 v18, s[12:13], s50, s50, 1.0
	v_rcp_f32_e32 v19, v18
	s_lshl_b32 s7, -1, s3
	s_not_b32 s74, s7
	s_add_i32 s7, s9, -1
	v_fma_f32 v24, -v18, v19, 1.0
	v_fmac_f32_e32 v19, v24, v19
	v_div_scale_f32 v24, vcc, 1.0, s50, 1.0
	v_mul_f32_e32 v25, v24, v19
	v_fma_f32 v26, -v18, v25, v24
	v_fmac_f32_e32 v25, v26, v19
	s_cmp_lg_u32 s11, 0
	v_fma_f32 v18, -v18, v25, v24
	s_waitcnt vmcnt(6)
	s_cselect_b32 s11, s7, -1
	v_div_fmas_f32 v18, v18, v19, v25
	s_cmp_eq_u32 s61, 2
	v_div_fixup_f32 v170, v18, s50, 1.0
	s_cselect_b64 s[12:13], -1, 0
	s_cmpk_gt_u32 s6, 0x17f
	v_mbcnt_lo_u32_b32 v18, -1, 0
	v_mov_b32_e32 v172, v170
	v_mov_b32_e32 v173, v170
	s_cselect_b64 s[28:29], -1, 0
	v_mov_b64_e32 v[174:175], s[4:5]
	v_mbcnt_hi_u32_b32 v167, -1, v18
	v_add_u32_e32 v169, 0, v20
	v_add_u32_e32 v178, 0, v21
	v_add_u32_e32 v179, 0, v23
	v_add_u32_e32 v180, 0, v22
	s_barrier
	s_branch .LBB6_8

.LBB6_15:
	s_add_u32 s82, s36, s20
	s_addc_u32 s83, s37, s21
	s_add_u32 s31, s36, 0x100
	s_addc_u32 s39, s37, 0
	s_and_b64 s[40:41], s[12:13], exec
	ds_read_b128 v[82:85], v169
	ds_read_b128 v[94:97], v169 offset:2048
	ds_read_b128 v[102:105], v178
	ds_read_b128 v[110:113], v178 offset:2048
	s_cselect_b32 s45, s5, s39
	s_cselect_b32 s44, s4, s31
	s_add_u32 s31, s34, 0x100
	s_addc_u32 s39, s35, 0
	s_and_b64 s[40:41], s[12:13], exec
	s_cselect_b32 s47, s7, s39
	s_cselect_b32 s46, s6, s31
	s_add_u32 s42, s44, 0x80
	s_addc_u32 s43, s45, 0
	s_add_u32 s40, s46, 0x80
	s_addc_u32 s41, s47, 0
	ds_read_b128 v[58:61], v179
	ds_read_b128 v[66:69], v179 offset:2048
	ds_read_b128 v[62:65], v180
	ds_read_b128 v[70:73], v180 offset:2048
	ds_read_b128 v[74:77], v179 offset:4096
	ds_read_b128 v[86:89], v179 offset:6144
	ds_read_b128 v[78:81], v180 offset:4096
	ds_read_b128 v[90:93], v180 offset:6144
	s_add_u32 s84, s82, 0x80
	s_addc_u32 s85, s83, 0
	s_mov_b32 m0, s68
	s_nop 0
	global_load_lds_dwordx4 v162, s[84:85] sc1
	s_mov_b32 m0, s69
	s_nop 0
	global_load_lds_dwordx4 v166, s[84:85] sc1
	s_waitcnt lgkmcnt(8)
	ds_read_b128 v[142:145], v169 offset:16384
	ds_read_b128 v[146:149], v169 offset:18432
	ds_read_b128 v[150:153], v178 offset:16384
	ds_read_b128 v[154:157], v178 offset:18432
	s_waitcnt vmcnt(8)
	s_waitcnt lgkmcnt(0)
	s_barrier
	s_waitcnt lgkmcnt(0)
	s_waitcnt vmcnt(16)
	v_mov_b32_e32 v171, v170
	v_pk_mul_f32 v[16:17], v[170:171], v[16:17]
	v_pk_mul_f32 v[14:15], v[172:173], v[14:15]
	v_pk_mul_f32 v[12:13], v[170:171], v[12:13]
	v_pk_mul_f32 v[10:11], v[172:173], v[10:11]
	v_pk_mul_f32 v[8:9], v[170:171], v[8:9]
	v_pk_mul_f32 v[6:7], v[172:173], v[6:7]
	v_pk_mul_f32 v[4:5], v[170:171], v[4:5]
	v_pk_mul_f32 v[2:3], v[172:173], v[2:3]
	s_setprio 1
	v_mfma_f32_16x16x128_f8f6f4 v[18:21], v[82:85], v[58:61], v[14:17] cbsz:4 blgp:4
	v_mfma_f32_16x16x128_f8f6f4 v[18:21], v[102:105], v[62:65], v[18:21] cbsz:4 blgp:4
	v_mfma_f32_16x16x128_f8f6f4 v[22:25], v[94:97], v[58:61], v[10:13] cbsz:4 blgp:4
	v_mfma_f32_16x16x128_f8f6f4 v[22:25], v[110:113], v[62:65], v[22:25] cbsz:4 blgp:4
	v_mfma_f32_16x16x128_f8f6f4 v[26:29], v[82:85], v[66:69], v[14:17] cbsz:4 blgp:4
	v_mfma_f32_16x16x128_f8f6f4 v[26:29], v[102:105], v[70:73], v[26:29] cbsz:4 blgp:4
	v_mfma_f32_16x16x128_f8f6f4 v[30:33], v[94:97], v[66:69], v[10:13] cbsz:4 blgp:4
	v_mfma_f32_16x16x128_f8f6f4 v[30:33], v[110:113], v[70:73], v[30:33] cbsz:4 blgp:4
	v_mfma_f32_16x16x128_f8f6f4 v[34:37], v[82:85], v[74:77], v[14:17] cbsz:4 blgp:4
	v_mfma_f32_16x16x128_f8f6f4 v[34:37], v[102:105], v[78:81], v[34:37] cbsz:4 blgp:4
	v_mfma_f32_16x16x128_f8f6f4 v[38:41], v[94:97], v[74:77], v[10:13] cbsz:4 blgp:4
	v_mfma_f32_16x16x128_f8f6f4 v[38:41], v[110:113], v[78:81], v[38:41] cbsz:4 blgp:4
	v_mfma_f32_16x16x128_f8f6f4 v[42:45], v[82:85], v[86:89], v[14:17] cbsz:4 blgp:4
	v_mfma_f32_16x16x128_f8f6f4 v[42:45], v[102:105], v[90:93], v[42:45] cbsz:4 blgp:4
	v_mfma_f32_16x16x128_f8f6f4 v[46:49], v[94:97], v[86:89], v[10:13] cbsz:4 blgp:4
	v_mfma_f32_16x16x128_f8f6f4 v[46:49], v[110:113], v[90:93], v[46:49] cbsz:4 blgp:4
	v_mfma_f32_16x16x128_f8f6f4 v[50:53], v[142:145], v[58:61], v[6:9] cbsz:4 blgp:4
	v_mfma_f32_16x16x128_f8f6f4 v[50:53], v[150:153], v[62:65], v[50:53] cbsz:4 blgp:4
	v_mfma_f32_16x16x128_f8f6f4 v[54:57], v[146:149], v[58:61], v[2:5] cbsz:4 blgp:4
	v_mfma_f32_16x16x128_f8f6f4 v[54:57], v[154:157], v[62:65], v[54:57] cbsz:4 blgp:4
	v_mfma_f32_16x16x128_f8f6f4 v[58:61], v[142:145], v[66:69], v[6:9] cbsz:4 blgp:4
	v_mfma_f32_16x16x128_f8f6f4 v[58:61], v[150:153], v[70:73], v[58:61] cbsz:4 blgp:4
	v_mfma_f32_16x16x128_f8f6f4 v[62:65], v[146:149], v[66:69], v[2:5] cbsz:4 blgp:4
	v_mfma_f32_16x16x128_f8f6f4 v[62:65], v[154:157], v[70:73], v[62:65] cbsz:4 blgp:4
	v_mfma_f32_16x16x128_f8f6f4 v[66:69], v[142:145], v[74:77], v[6:9] cbsz:4 blgp:4
	v_mfma_f32_16x16x128_f8f6f4 v[66:69], v[150:153], v[78:81], v[66:69] cbsz:4 blgp:4
	v_mfma_f32_16x16x128_f8f6f4 v[70:73], v[146:149], v[74:77], v[2:5] cbsz:4 blgp:4
	v_mfma_f32_16x16x128_f8f6f4 v[70:73], v[154:157], v[78:81], v[70:73] cbsz:4 blgp:4
	v_mfma_f32_16x16x128_f8f6f4 v[74:77], v[142:145], v[86:89], v[6:9] cbsz:4 blgp:4
	v_mfma_f32_16x16x128_f8f6f4 v[74:77], v[150:153], v[90:93], v[74:77] cbsz:4 blgp:4
	v_mfma_f32_16x16x128_f8f6f4 v[78:81], v[146:149], v[86:89], v[2:5] cbsz:4 blgp:4
	v_mfma_f32_16x16x128_f8f6f4 v[78:81], v[154:157], v[90:93], v[78:81] cbsz:4 blgp:4
	s_setprio 0
	s_barrier
	s_mov_b32 m0, s54
	s_nop 0
	global_load_lds_dwordx4 v164, s[46:47] sc1
	s_mov_b32 m0, s55
	s_nop 0
	global_load_lds_dwordx4 v168, s[46:47] sc1
	ds_read_b128 v[114:117], v179 offset:16384
	ds_read_b128 v[122:125], v179 offset:18432
	ds_read_b128 v[130:133], v180 offset:16384
	ds_read_b128 v[134:137], v180 offset:18432
	ds_read_b128 v[158:161], v179 offset:20480
	ds_read_b128 v[182:185], v179 offset:22528
	ds_read_b128 v[186:189], v180 offset:20480
	ds_read_b128 v[190:193], v180 offset:22528
	s_mov_b32 m0, s53
	s_nop 0
	global_load_lds_dwordx4 v162, s[44:45] sc1
	s_mov_b32 m0, s56
	s_nop 0
	global_load_lds_dwordx4 v166, s[44:45] sc1
	s_add_u32 s46, s46, s22
	s_addc_u32 s47, s47, s23
	s_mov_b32 m0, s57
	s_nop 0
	global_load_lds_dwordx4 v164, s[46:47] sc1
	s_mov_b32 m0, s58
	s_nop 0
	global_load_lds_dwordx4 v168, s[46:47] sc1
	s_waitcnt vmcnt(8)
	s_waitcnt lgkmcnt(0)
	s_barrier
	s_setprio 1
	v_mfma_f32_16x16x128_f8f6f4 v[86:89], v[82:85], v[114:117], v[14:17] cbsz:4 blgp:4
	v_mfma_f32_16x16x128_f8f6f4 v[86:89], v[102:105], v[130:133], v[86:89] cbsz:4 blgp:4
	v_mfma_f32_16x16x128_f8f6f4 v[90:93], v[94:97], v[114:117], v[10:13] cbsz:4 blgp:4
	v_mfma_f32_16x16x128_f8f6f4 v[90:93], v[110:113], v[130:133], v[90:93] cbsz:4 blgp:4
	v_mfma_f32_16x16x128_f8f6f4 v[98:101], v[82:85], v[122:125], v[14:17] cbsz:4 blgp:4
	v_mfma_f32_16x16x128_f8f6f4 v[98:101], v[102:105], v[134:137], v[98:101] cbsz:4 blgp:4
	v_mfma_f32_16x16x128_f8f6f4 v[106:109], v[94:97], v[122:125], v[10:13] cbsz:4 blgp:4
	v_mfma_f32_16x16x128_f8f6f4 v[106:109], v[110:113], v[134:137], v[106:109] cbsz:4 blgp:4
	v_mfma_f32_16x16x128_f8f6f4 v[118:121], v[82:85], v[158:161], v[14:17] cbsz:4 blgp:4
	v_mfma_f32_16x16x128_f8f6f4 v[118:121], v[102:105], v[186:189], v[118:121] cbsz:4 blgp:4
	v_mfma_f32_16x16x128_f8f6f4 v[126:129], v[94:97], v[158:161], v[10:13] cbsz:4 blgp:4
	v_mfma_f32_16x16x128_f8f6f4 v[126:129], v[110:113], v[186:189], v[126:129] cbsz:4 blgp:4
	v_mfma_f32_16x16x128_f8f6f4 v[138:141], v[82:85], v[182:185], v[14:17] cbsz:4 blgp:4
	v_mfma_f32_16x16x128_f8f6f4 v[138:141], v[102:105], v[190:193], v[138:141] cbsz:4 blgp:4
	v_mfma_f32_16x16x128_f8f6f4 v[82:85], v[94:97], v[182:185], v[10:13] cbsz:4 blgp:4
	v_mfma_f32_16x16x128_f8f6f4 v[82:85], v[110:113], v[190:193], v[82:85] cbsz:4 blgp:4
	v_mfma_f32_16x16x128_f8f6f4 v[94:97], v[142:145], v[114:117], v[6:9] cbsz:4 blgp:4
	v_mfma_f32_16x16x128_f8f6f4 v[94:97], v[150:153], v[130:133], v[94:97] cbsz:4 blgp:4
	v_mfma_f32_16x16x128_f8f6f4 v[102:105], v[146:149], v[114:117], v[2:5] cbsz:4 blgp:4
	v_mfma_f32_16x16x128_f8f6f4 v[102:105], v[154:157], v[130:133], v[102:105] cbsz:4 blgp:4
	v_mfma_f32_16x16x128_f8f6f4 v[110:113], v[142:145], v[122:125], v[6:9] cbsz:4 blgp:4
	v_mfma_f32_16x16x128_f8f6f4 v[110:113], v[150:153], v[134:137], v[110:113] cbsz:4 blgp:4
	v_mfma_f32_16x16x128_f8f6f4 v[114:117], v[146:149], v[122:125], v[2:5] cbsz:4 blgp:4
	v_mfma_f32_16x16x128_f8f6f4 v[114:117], v[154:157], v[134:137], v[114:117] cbsz:4 blgp:4
	v_mfma_f32_16x16x128_f8f6f4 v[122:125], v[142:145], v[158:161], v[6:9] cbsz:4 blgp:4
	v_mfma_f32_16x16x128_f8f6f4 v[122:125], v[150:153], v[186:189], v[122:125] cbsz:4 blgp:4
	v_mfma_f32_16x16x128_f8f6f4 v[130:133], v[146:149], v[158:161], v[2:5] cbsz:4 blgp:4
	v_mfma_f32_16x16x128_f8f6f4 v[130:133], v[154:157], v[186:189], v[130:133] cbsz:4 blgp:4
	v_mfma_f32_16x16x128_f8f6f4 v[134:137], v[142:145], v[182:185], v[6:9] cbsz:4 blgp:4
	v_mfma_f32_16x16x128_f8f6f4 v[134:137], v[150:153], v[190:193], v[134:137] cbsz:4 blgp:4
	v_mfma_f32_16x16x128_f8f6f4 v[142:145], v[146:149], v[182:185], v[2:5] cbsz:4 blgp:4
	v_mfma_f32_16x16x128_f8f6f4 v[142:145], v[154:157], v[190:193], v[142:145] cbsz:4 blgp:4
	s_setprio 0
	s_barrier
	ds_read_b128 v[146:149], v169 offset:32768
	ds_read_b128 v[150:153], v169 offset:34816
	ds_read_b128 v[154:157], v178 offset:32768
	ds_read_b128 v[158:161], v178 offset:34816
	ds_read_b128 v[182:185], v179 offset:32768
	ds_read_b128 v[186:189], v179 offset:34816
	ds_read_b128 v[190:193], v180 offset:32768
	ds_read_b128 v[194:197], v180 offset:34816
	ds_read_b128 v[198:201], v179 offset:36864
	ds_read_b128 v[202:205], v179 offset:38912
	ds_read_b128 v[206:209], v180 offset:36864
	ds_read_b128 v[210:213], v180 offset:38912
	s_add_u32 s44, s44, s20
	s_addc_u32 s45, s45, s21
	s_mov_b32 m0, s59
	s_nop 0
	global_load_lds_dwordx4 v162, s[44:45] sc1
	s_mov_b32 m0, s60
	s_nop 0
	global_load_lds_dwordx4 v166, s[44:45] sc1
	s_waitcnt lgkmcnt(8)
	ds_read_b128 v[214:217], v169 offset:49152
	ds_read_b128 v[218:221], v169 offset:51200
	ds_read_b128 v[222:225], v178 offset:49152
	ds_read_b128 v[226:229], v178 offset:51200
	s_waitcnt vmcnt(8)
	s_waitcnt lgkmcnt(0)
	s_barrier
	s_waitcnt lgkmcnt(0)
	s_setprio 1
	v_mfma_f32_16x16x128_f8f6f4 v[18:21], v[146:149], v[182:185], v[18:21] cbsz:4 blgp:4
	v_mfma_f32_16x16x128_f8f6f4 v[18:21], v[154:157], v[190:193], v[18:21] cbsz:4 blgp:4
	v_mfma_f32_16x16x128_f8f6f4 v[22:25], v[150:153], v[182:185], v[22:25] cbsz:4 blgp:4
	v_mfma_f32_16x16x128_f8f6f4 v[22:25], v[158:161], v[190:193], v[22:25] cbsz:4 blgp:4
	v_mfma_f32_16x16x128_f8f6f4 v[26:29], v[146:149], v[186:189], v[26:29] cbsz:4 blgp:4
	v_mfma_f32_16x16x128_f8f6f4 v[26:29], v[154:157], v[194:197], v[26:29] cbsz:4 blgp:4
	v_mfma_f32_16x16x128_f8f6f4 v[30:33], v[150:153], v[186:189], v[30:33] cbsz:4 blgp:4
	v_mfma_f32_16x16x128_f8f6f4 v[30:33], v[158:161], v[194:197], v[30:33] cbsz:4 blgp:4
	v_mfma_f32_16x16x128_f8f6f4 v[34:37], v[146:149], v[198:201], v[34:37] cbsz:4 blgp:4
	v_mfma_f32_16x16x128_f8f6f4 v[34:37], v[154:157], v[206:209], v[34:37] cbsz:4 blgp:4
	v_mfma_f32_16x16x128_f8f6f4 v[38:41], v[150:153], v[198:201], v[38:41] cbsz:4 blgp:4
	v_mfma_f32_16x16x128_f8f6f4 v[38:41], v[158:161], v[206:209], v[38:41] cbsz:4 blgp:4
	v_mfma_f32_16x16x128_f8f6f4 v[42:45], v[146:149], v[202:205], v[42:45] cbsz:4 blgp:4
	v_mfma_f32_16x16x128_f8f6f4 v[42:45], v[154:157], v[210:213], v[42:45] cbsz:4 blgp:4
	v_mfma_f32_16x16x128_f8f6f4 v[46:49], v[150:153], v[202:205], v[46:49] cbsz:4 blgp:4
	v_mfma_f32_16x16x128_f8f6f4 v[46:49], v[158:161], v[210:213], v[46:49] cbsz:4 blgp:4
	v_mfma_f32_16x16x128_f8f6f4 v[50:53], v[214:217], v[182:185], v[50:53] cbsz:4 blgp:4
	v_mfma_f32_16x16x128_f8f6f4 v[50:53], v[222:225], v[190:193], v[50:53] cbsz:4 blgp:4
	v_mfma_f32_16x16x128_f8f6f4 v[54:57], v[218:221], v[182:185], v[54:57] cbsz:4 blgp:4
	v_mfma_f32_16x16x128_f8f6f4 v[54:57], v[226:229], v[190:193], v[54:57] cbsz:4 blgp:4
	v_mfma_f32_16x16x128_f8f6f4 v[58:61], v[214:217], v[186:189], v[58:61] cbsz:4 blgp:4
	v_mfma_f32_16x16x128_f8f6f4 v[58:61], v[222:225], v[194:197], v[58:61] cbsz:4 blgp:4
	v_mfma_f32_16x16x128_f8f6f4 v[62:65], v[218:221], v[186:189], v[62:65] cbsz:4 blgp:4
	v_mfma_f32_16x16x128_f8f6f4 v[62:65], v[226:229], v[194:197], v[62:65] cbsz:4 blgp:4
	v_mfma_f32_16x16x128_f8f6f4 v[66:69], v[214:217], v[198:201], v[66:69] cbsz:4 blgp:4
	v_mfma_f32_16x16x128_f8f6f4 v[66:69], v[222:225], v[206:209], v[66:69] cbsz:4 blgp:4
	v_mfma_f32_16x16x128_f8f6f4 v[70:73], v[218:221], v[198:201], v[70:73] cbsz:4 blgp:4
	v_mfma_f32_16x16x128_f8f6f4 v[70:73], v[226:229], v[206:209], v[70:73] cbsz:4 blgp:4
	v_mfma_f32_16x16x128_f8f6f4 v[74:77], v[214:217], v[202:205], v[74:77] cbsz:4 blgp:4
	v_mfma_f32_16x16x128_f8f6f4 v[74:77], v[222:225], v[210:213], v[74:77] cbsz:4 blgp:4
	v_mfma_f32_16x16x128_f8f6f4 v[78:81], v[218:221], v[202:205], v[78:81] cbsz:4 blgp:4
	v_mfma_f32_16x16x128_f8f6f4 v[78:81], v[226:229], v[210:213], v[78:81] cbsz:4 blgp:4
	s_setprio 0
	s_barrier
	s_mov_b32 m0, s62
	s_nop 0
	global_load_lds_dwordx4 v164, s[40:41] sc1
	s_mov_b32 m0, s63
	s_nop 0
	global_load_lds_dwordx4 v168, s[40:41] sc1
	ds_read_b128 v[182:185], v179 offset:49152
	ds_read_b128 v[186:189], v179 offset:51200
	ds_read_b128 v[190:193], v180 offset:49152
	ds_read_b128 v[194:197], v180 offset:51200
	ds_read_b128 v[198:201], v179 offset:53248
	ds_read_b128 v[202:205], v179 offset:55296
	ds_read_b128 v[206:209], v180 offset:53248
	ds_read_b128 v[210:213], v180 offset:55296
	s_mov_b32 m0, s64
	s_nop 0
	global_load_lds_dwordx4 v162, s[42:43] sc1
	s_mov_b32 m0, s65
	s_nop 0
	global_load_lds_dwordx4 v166, s[42:43] sc1
	s_add_u32 s40, s40, s22
	s_addc_u32 s41, s41, s23
	s_mov_b32 m0, s66
	s_nop 0
	global_load_lds_dwordx4 v164, s[40:41] sc1
	s_mov_b32 m0, s67
	s_nop 0
	global_load_lds_dwordx4 v168, s[40:41] sc1
	s_waitcnt vmcnt(8)
	s_waitcnt lgkmcnt(0)
	s_barrier
	s_setprio 1
	v_mfma_f32_16x16x128_f8f6f4 v[86:89], v[146:149], v[182:185], v[86:89] cbsz:4 blgp:4
	v_mfma_f32_16x16x128_f8f6f4 v[86:89], v[154:157], v[190:193], v[86:89] cbsz:4 blgp:4
	v_mfma_f32_16x16x128_f8f6f4 v[90:93], v[150:153], v[182:185], v[90:93] cbsz:4 blgp:4
	v_mfma_f32_16x16x128_f8f6f4 v[90:93], v[158:161], v[190:193], v[90:93] cbsz:4 blgp:4
	v_mfma_f32_16x16x128_f8f6f4 v[98:101], v[146:149], v[186:189], v[98:101] cbsz:4 blgp:4
	v_mfma_f32_16x16x128_f8f6f4 v[98:101], v[154:157], v[194:197], v[98:101] cbsz:4 blgp:4
	v_mfma_f32_16x16x128_f8f6f4 v[106:109], v[150:153], v[186:189], v[106:109] cbsz:4 blgp:4
	v_mfma_f32_16x16x128_f8f6f4 v[106:109], v[158:161], v[194:197], v[106:109] cbsz:4 blgp:4
	v_mfma_f32_16x16x128_f8f6f4 v[118:121], v[146:149], v[198:201], v[118:121] cbsz:4 blgp:4
	v_mfma_f32_16x16x128_f8f6f4 v[118:121], v[154:157], v[206:209], v[118:121] cbsz:4 blgp:4
	v_mfma_f32_16x16x128_f8f6f4 v[126:129], v[150:153], v[198:201], v[126:129] cbsz:4 blgp:4
	v_mfma_f32_16x16x128_f8f6f4 v[126:129], v[158:161], v[206:209], v[126:129] cbsz:4 blgp:4
	v_mfma_f32_16x16x128_f8f6f4 v[138:141], v[146:149], v[202:205], v[138:141] cbsz:4 blgp:4
	v_mfma_f32_16x16x128_f8f6f4 v[138:141], v[154:157], v[210:213], v[138:141] cbsz:4 blgp:4
	v_mfma_f32_16x16x128_f8f6f4 v[82:85], v[150:153], v[202:205], v[82:85] cbsz:4 blgp:4
	v_mfma_f32_16x16x128_f8f6f4 v[82:85], v[158:161], v[210:213], v[82:85] cbsz:4 blgp:4
	v_mfma_f32_16x16x128_f8f6f4 v[94:97], v[214:217], v[182:185], v[94:97] cbsz:4 blgp:4
	v_mfma_f32_16x16x128_f8f6f4 v[94:97], v[222:225], v[190:193], v[94:97] cbsz:4 blgp:4
	v_mfma_f32_16x16x128_f8f6f4 v[102:105], v[218:221], v[182:185], v[102:105] cbsz:4 blgp:4
	v_mfma_f32_16x16x128_f8f6f4 v[102:105], v[226:229], v[190:193], v[102:105] cbsz:4 blgp:4
	v_mfma_f32_16x16x128_f8f6f4 v[110:113], v[214:217], v[186:189], v[110:113] cbsz:4 blgp:4
	v_mfma_f32_16x16x128_f8f6f4 v[110:113], v[222:225], v[194:197], v[110:113] cbsz:4 blgp:4
	v_mfma_f32_16x16x128_f8f6f4 v[114:117], v[218:221], v[186:189], v[114:117] cbsz:4 blgp:4
	v_mfma_f32_16x16x128_f8f6f4 v[114:117], v[226:229], v[194:197], v[114:117] cbsz:4 blgp:4
	v_mfma_f32_16x16x128_f8f6f4 v[122:125], v[214:217], v[198:201], v[122:125] cbsz:4 blgp:4
	v_mfma_f32_16x16x128_f8f6f4 v[122:125], v[222:225], v[206:209], v[122:125] cbsz:4 blgp:4
	v_mfma_f32_16x16x128_f8f6f4 v[130:133], v[218:221], v[198:201], v[130:133] cbsz:4 blgp:4
	v_mfma_f32_16x16x128_f8f6f4 v[130:133], v[226:229], v[206:209], v[130:133] cbsz:4 blgp:4
	v_mfma_f32_16x16x128_f8f6f4 v[134:137], v[214:217], v[202:205], v[134:137] cbsz:4 blgp:4
	v_mfma_f32_16x16x128_f8f6f4 v[134:137], v[222:225], v[210:213], v[134:137] cbsz:4 blgp:4
	v_mfma_f32_16x16x128_f8f6f4 v[142:145], v[218:221], v[202:205], v[142:145] cbsz:4 blgp:4
	v_mfma_f32_16x16x128_f8f6f4 v[142:145], v[226:229], v[210:213], v[142:145] cbsz:4 blgp:4
	s_setprio 0
	s_andn2_b64 vcc, exec, s[28:29]
	s_barrier
	s_cbranch_vccnz .LBB6_20
	s_ashr_i32 s39, s38, 31
	s_lshl_b64 s[38:39], s[38:39], 10
	s_add_u32 s38, s14, s38
	s_addc_u32 s39, s15, s39
	s_add_u32 s31, s36, 0x200
	s_addc_u32 s46, s37, 0
	s_add_u32 s47, s34, 0x200
	s_addc_u32 s81, s35, 0
	s_add_u32 s34, s82, 0x180
	s_addc_u32 s35, s83, 0
	s_mov_b32 s82, 4
	s_cmp_eq_u32 s61, s82
	s_cselect_b64 s[36:37], -1, 0
	s_cmp_lg_u32 s61, s82
	s_cbranch_scc1 .LBB6_18

.LBB6_18:
	ds_read_b128 v[146:149], v169
	ds_read_b128 v[150:153], v169 offset:2048
	ds_read_b128 v[154:157], v178
	ds_read_b128 v[158:161], v178 offset:2048
	s_and_b64 s[36:37], s[36:37], exec
	s_cselect_b32 s42, s4, s31
	s_cselect_b32 s43, s5, s46
	s_cselect_b32 s45, s7, s81
	s_cselect_b32 s44, s6, s47
	s_add_u32 s40, s42, 0x80
	s_addc_u32 s41, s43, 0
	s_add_u32 s36, s44, 0x80
	s_addc_u32 s37, s45, 0
	ds_read_b128 v[182:185], v179
	ds_read_b128 v[186:189], v179 offset:2048
	ds_read_b128 v[190:193], v180
	ds_read_b128 v[194:197], v180 offset:2048
	ds_read_b128 v[198:201], v179 offset:4096
	ds_read_b128 v[202:205], v179 offset:6144
	ds_read_b128 v[206:209], v180 offset:4096
	ds_read_b128 v[210:213], v180 offset:6144
	s_mov_b32 m0, s68
	s_nop 0
	global_load_lds_dwordx4 v162, s[34:35] sc1
	s_mov_b32 m0, s69
	s_nop 0
	global_load_lds_dwordx4 v166, s[34:35] sc1
	s_waitcnt lgkmcnt(8)
	ds_read_b128 v[214:217], v169 offset:16384
	ds_read_b128 v[218:221], v169 offset:18432
	ds_read_b128 v[222:225], v178 offset:16384
	ds_read_b128 v[226:229], v178 offset:18432
	s_waitcnt vmcnt(8)
	s_waitcnt lgkmcnt(0)
	s_barrier
	s_waitcnt lgkmcnt(0)
	s_setprio 1
	v_mfma_f32_16x16x128_f8f6f4 v[18:21], v[146:149], v[182:185], v[18:21] cbsz:4 blgp:4
	v_mfma_f32_16x16x128_f8f6f4 v[18:21], v[154:157], v[190:193], v[18:21] cbsz:4 blgp:4
	v_mfma_f32_16x16x128_f8f6f4 v[22:25], v[150:153], v[182:185], v[22:25] cbsz:4 blgp:4
	v_mfma_f32_16x16x128_f8f6f4 v[22:25], v[158:161], v[190:193], v[22:25] cbsz:4 blgp:4
	v_mfma_f32_16x16x128_f8f6f4 v[26:29], v[146:149], v[186:189], v[26:29] cbsz:4 blgp:4
	v_mfma_f32_16x16x128_f8f6f4 v[26:29], v[154:157], v[194:197], v[26:29] cbsz:4 blgp:4
	v_mfma_f32_16x16x128_f8f6f4 v[30:33], v[150:153], v[186:189], v[30:33] cbsz:4 blgp:4
	v_mfma_f32_16x16x128_f8f6f4 v[30:33], v[158:161], v[194:197], v[30:33] cbsz:4 blgp:4
	v_mfma_f32_16x16x128_f8f6f4 v[34:37], v[146:149], v[198:201], v[34:37] cbsz:4 blgp:4
	v_mfma_f32_16x16x128_f8f6f4 v[34:37], v[154:157], v[206:209], v[34:37] cbsz:4 blgp:4
	v_mfma_f32_16x16x128_f8f6f4 v[38:41], v[150:153], v[198:201], v[38:41] cbsz:4 blgp:4
	v_mfma_f32_16x16x128_f8f6f4 v[38:41], v[158:161], v[206:209], v[38:41] cbsz:4 blgp:4
	v_mfma_f32_16x16x128_f8f6f4 v[42:45], v[146:149], v[202:205], v[42:45] cbsz:4 blgp:4
	v_mfma_f32_16x16x128_f8f6f4 v[42:45], v[154:157], v[210:213], v[42:45] cbsz:4 blgp:4
	v_mfma_f32_16x16x128_f8f6f4 v[46:49], v[150:153], v[202:205], v[46:49] cbsz:4 blgp:4
	v_mfma_f32_16x16x128_f8f6f4 v[46:49], v[158:161], v[210:213], v[46:49] cbsz:4 blgp:4
	v_mfma_f32_16x16x128_f8f6f4 v[50:53], v[214:217], v[182:185], v[50:53] cbsz:4 blgp:4
	v_mfma_f32_16x16x128_f8f6f4 v[50:53], v[222:225], v[190:193], v[50:53] cbsz:4 blgp:4
	v_mfma_f32_16x16x128_f8f6f4 v[54:57], v[218:221], v[182:185], v[54:57] cbsz:4 blgp:4
	v_mfma_f32_16x16x128_f8f6f4 v[54:57], v[226:229], v[190:193], v[54:57] cbsz:4 blgp:4
	v_mfma_f32_16x16x128_f8f6f4 v[58:61], v[214:217], v[186:189], v[58:61] cbsz:4 blgp:4
	v_mfma_f32_16x16x128_f8f6f4 v[58:61], v[222:225], v[194:197], v[58:61] cbsz:4 blgp:4
	v_mfma_f32_16x16x128_f8f6f4 v[62:65], v[218:221], v[186:189], v[62:65] cbsz:4 blgp:4
	v_mfma_f32_16x16x128_f8f6f4 v[62:65], v[226:229], v[194:197], v[62:65] cbsz:4 blgp:4
	v_mfma_f32_16x16x128_f8f6f4 v[66:69], v[214:217], v[198:201], v[66:69] cbsz:4 blgp:4
	v_mfma_f32_16x16x128_f8f6f4 v[66:69], v[222:225], v[206:209], v[66:69] cbsz:4 blgp:4
	v_mfma_f32_16x16x128_f8f6f4 v[70:73], v[218:221], v[198:201], v[70:73] cbsz:4 blgp:4
	v_mfma_f32_16x16x128_f8f6f4 v[70:73], v[226:229], v[206:209], v[70:73] cbsz:4 blgp:4
	v_mfma_f32_16x16x128_f8f6f4 v[74:77], v[214:217], v[202:205], v[74:77] cbsz:4 blgp:4
	v_mfma_f32_16x16x128_f8f6f4 v[74:77], v[222:225], v[210:213], v[74:77] cbsz:4 blgp:4
	v_mfma_f32_16x16x128_f8f6f4 v[78:81], v[218:221], v[202:205], v[78:81] cbsz:4 blgp:4
	v_mfma_f32_16x16x128_f8f6f4 v[78:81], v[226:229], v[210:213], v[78:81] cbsz:4 blgp:4
	s_setprio 0
	s_barrier
	s_mov_b32 m0, s54
	s_nop 0
	global_load_lds_dwordx4 v164, s[44:45] sc1
	s_mov_b32 m0, s55
	s_nop 0
	global_load_lds_dwordx4 v168, s[44:45] sc1
	ds_read_b128 v[182:185], v179 offset:16384
	ds_read_b128 v[186:189], v179 offset:18432
	ds_read_b128 v[190:193], v180 offset:16384
	ds_read_b128 v[194:197], v180 offset:18432
	ds_read_b128 v[198:201], v179 offset:20480
	ds_read_b128 v[202:205], v179 offset:22528
	ds_read_b128 v[206:209], v180 offset:20480
	ds_read_b128 v[210:213], v180 offset:22528
	s_mov_b32 m0, s53
	s_nop 0
	global_load_lds_dwordx4 v162, s[42:43] sc1
	s_mov_b32 m0, s56
	s_nop 0
	global_load_lds_dwordx4 v166, s[42:43] sc1
	s_add_u32 s44, s44, s22
	s_addc_u32 s45, s45, s23
	s_mov_b32 m0, s57
	s_nop 0
	global_load_lds_dwordx4 v164, s[44:45] sc1
	s_mov_b32 m0, s58
	s_nop 0
	global_load_lds_dwordx4 v168, s[44:45] sc1
	s_waitcnt vmcnt(8)
	s_waitcnt lgkmcnt(0)
	s_barrier
	s_setprio 1
	v_mfma_f32_16x16x128_f8f6f4 v[86:89], v[146:149], v[182:185], v[86:89] cbsz:4 blgp:4
	v_mfma_f32_16x16x128_f8f6f4 v[86:89], v[154:157], v[190:193], v[86:89] cbsz:4 blgp:4
	v_mfma_f32_16x16x128_f8f6f4 v[90:93], v[150:153], v[182:185], v[90:93] cbsz:4 blgp:4
	v_mfma_f32_16x16x128_f8f6f4 v[90:93], v[158:161], v[190:193], v[90:93] cbsz:4 blgp:4
	v_mfma_f32_16x16x128_f8f6f4 v[98:101], v[146:149], v[186:189], v[98:101] cbsz:4 blgp:4
	v_mfma_f32_16x16x128_f8f6f4 v[98:101], v[154:157], v[194:197], v[98:101] cbsz:4 blgp:4
	v_mfma_f32_16x16x128_f8f6f4 v[106:109], v[150:153], v[186:189], v[106:109] cbsz:4 blgp:4
	v_mfma_f32_16x16x128_f8f6f4 v[106:109], v[158:161], v[194:197], v[106:109] cbsz:4 blgp:4
	v_mfma_f32_16x16x128_f8f6f4 v[118:121], v[146:149], v[198:201], v[118:121] cbsz:4 blgp:4
	v_mfma_f32_16x16x128_f8f6f4 v[118:121], v[154:157], v[206:209], v[118:121] cbsz:4 blgp:4
	v_mfma_f32_16x16x128_f8f6f4 v[126:129], v[150:153], v[198:201], v[126:129] cbsz:4 blgp:4
	v_mfma_f32_16x16x128_f8f6f4 v[126:129], v[158:161], v[206:209], v[126:129] cbsz:4 blgp:4
	v_mfma_f32_16x16x128_f8f6f4 v[138:141], v[146:149], v[202:205], v[138:141] cbsz:4 blgp:4
	v_mfma_f32_16x16x128_f8f6f4 v[138:141], v[154:157], v[210:213], v[138:141] cbsz:4 blgp:4
	v_mfma_f32_16x16x128_f8f6f4 v[82:85], v[150:153], v[202:205], v[82:85] cbsz:4 blgp:4
	v_mfma_f32_16x16x128_f8f6f4 v[82:85], v[158:161], v[210:213], v[82:85] cbsz:4 blgp:4
	v_mfma_f32_16x16x128_f8f6f4 v[94:97], v[214:217], v[182:185], v[94:97] cbsz:4 blgp:4
	v_mfma_f32_16x16x128_f8f6f4 v[94:97], v[222:225], v[190:193], v[94:97] cbsz:4 blgp:4
	v_mfma_f32_16x16x128_f8f6f4 v[102:105], v[218:221], v[182:185], v[102:105] cbsz:4 blgp:4
	v_mfma_f32_16x16x128_f8f6f4 v[102:105], v[226:229], v[190:193], v[102:105] cbsz:4 blgp:4
	v_mfma_f32_16x16x128_f8f6f4 v[110:113], v[214:217], v[186:189], v[110:113] cbsz:4 blgp:4
	v_mfma_f32_16x16x128_f8f6f4 v[110:113], v[222:225], v[194:197], v[110:113] cbsz:4 blgp:4
	v_mfma_f32_16x16x128_f8f6f4 v[114:117], v[218:221], v[186:189], v[114:117] cbsz:4 blgp:4
	v_mfma_f32_16x16x128_f8f6f4 v[114:117], v[226:229], v[194:197], v[114:117] cbsz:4 blgp:4
	v_mfma_f32_16x16x128_f8f6f4 v[122:125], v[214:217], v[198:201], v[122:125] cbsz:4 blgp:4
	v_mfma_f32_16x16x128_f8f6f4 v[122:125], v[222:225], v[206:209], v[122:125] cbsz:4 blgp:4
	v_mfma_f32_16x16x128_f8f6f4 v[130:133], v[218:221], v[198:201], v[130:133] cbsz:4 blgp:4
	v_mfma_f32_16x16x128_f8f6f4 v[130:133], v[226:229], v[206:209], v[130:133] cbsz:4 blgp:4
	v_mfma_f32_16x16x128_f8f6f4 v[134:137], v[214:217], v[202:205], v[134:137] cbsz:4 blgp:4
	v_mfma_f32_16x16x128_f8f6f4 v[134:137], v[222:225], v[210:213], v[134:137] cbsz:4 blgp:4
	v_mfma_f32_16x16x128_f8f6f4 v[142:145], v[218:221], v[202:205], v[142:145] cbsz:4 blgp:4
	v_mfma_f32_16x16x128_f8f6f4 v[142:145], v[226:229], v[210:213], v[142:145] cbsz:4 blgp:4
	s_setprio 0
	s_barrier
	ds_read_b128 v[146:149], v169 offset:32768
	ds_read_b128 v[150:153], v169 offset:34816
	ds_read_b128 v[154:157], v178 offset:32768
	ds_read_b128 v[158:161], v178 offset:34816
	ds_read_b128 v[182:185], v179 offset:32768
	ds_read_b128 v[186:189], v179 offset:34816
	ds_read_b128 v[190:193], v180 offset:32768
	ds_read_b128 v[194:197], v180 offset:34816
	ds_read_b128 v[198:201], v179 offset:36864
	ds_read_b128 v[202:205], v179 offset:38912
	ds_read_b128 v[206:209], v180 offset:36864
	ds_read_b128 v[210:213], v180 offset:38912
	s_add_u32 s42, s42, s20
	s_addc_u32 s43, s43, s21
	s_mov_b32 m0, s59
	s_nop 0
	global_load_lds_dwordx4 v162, s[42:43] sc1
	s_mov_b32 m0, s60
	s_nop 0
	global_load_lds_dwordx4 v166, s[42:43] sc1
	s_waitcnt lgkmcnt(8)
	ds_read_b128 v[214:217], v169 offset:49152
	ds_read_b128 v[218:221], v169 offset:51200
	ds_read_b128 v[222:225], v178 offset:49152
	ds_read_b128 v[226:229], v178 offset:51200
	s_waitcnt vmcnt(8)
	s_waitcnt lgkmcnt(0)
	s_barrier
	s_waitcnt lgkmcnt(0)
	s_setprio 1
	v_mfma_f32_16x16x128_f8f6f4 v[18:21], v[146:149], v[182:185], v[18:21] cbsz:4 blgp:4
	v_mfma_f32_16x16x128_f8f6f4 v[18:21], v[154:157], v[190:193], v[18:21] cbsz:4 blgp:4
	v_mfma_f32_16x16x128_f8f6f4 v[22:25], v[150:153], v[182:185], v[22:25] cbsz:4 blgp:4
	v_mfma_f32_16x16x128_f8f6f4 v[22:25], v[158:161], v[190:193], v[22:25] cbsz:4 blgp:4
	v_mfma_f32_16x16x128_f8f6f4 v[26:29], v[146:149], v[186:189], v[26:29] cbsz:4 blgp:4
	v_mfma_f32_16x16x128_f8f6f4 v[26:29], v[154:157], v[194:197], v[26:29] cbsz:4 blgp:4
	v_mfma_f32_16x16x128_f8f6f4 v[30:33], v[150:153], v[186:189], v[30:33] cbsz:4 blgp:4
	v_mfma_f32_16x16x128_f8f6f4 v[30:33], v[158:161], v[194:197], v[30:33] cbsz:4 blgp:4
	v_mfma_f32_16x16x128_f8f6f4 v[34:37], v[146:149], v[198:201], v[34:37] cbsz:4 blgp:4
	v_mfma_f32_16x16x128_f8f6f4 v[34:37], v[154:157], v[206:209], v[34:37] cbsz:4 blgp:4
	v_mfma_f32_16x16x128_f8f6f4 v[38:41], v[150:153], v[198:201], v[38:41] cbsz:4 blgp:4
	v_mfma_f32_16x16x128_f8f6f4 v[38:41], v[158:161], v[206:209], v[38:41] cbsz:4 blgp:4
	v_mfma_f32_16x16x128_f8f6f4 v[42:45], v[146:149], v[202:205], v[42:45] cbsz:4 blgp:4
	v_mfma_f32_16x16x128_f8f6f4 v[42:45], v[154:157], v[210:213], v[42:45] cbsz:4 blgp:4
	v_mfma_f32_16x16x128_f8f6f4 v[46:49], v[150:153], v[202:205], v[46:49] cbsz:4 blgp:4
	v_mfma_f32_16x16x128_f8f6f4 v[46:49], v[158:161], v[210:213], v[46:49] cbsz:4 blgp:4
	v_mfma_f32_16x16x128_f8f6f4 v[50:53], v[214:217], v[182:185], v[50:53] cbsz:4 blgp:4
	v_mfma_f32_16x16x128_f8f6f4 v[50:53], v[222:225], v[190:193], v[50:53] cbsz:4 blgp:4
	v_mfma_f32_16x16x128_f8f6f4 v[54:57], v[218:221], v[182:185], v[54:57] cbsz:4 blgp:4
	v_mfma_f32_16x16x128_f8f6f4 v[54:57], v[226:229], v[190:193], v[54:57] cbsz:4 blgp:4
	v_mfma_f32_16x16x128_f8f6f4 v[58:61], v[214:217], v[186:189], v[58:61] cbsz:4 blgp:4
	v_mfma_f32_16x16x128_f8f6f4 v[58:61], v[222:225], v[194:197], v[58:61] cbsz:4 blgp:4
	v_mfma_f32_16x16x128_f8f6f4 v[62:65], v[218:221], v[186:189], v[62:65] cbsz:4 blgp:4
	v_mfma_f32_16x16x128_f8f6f4 v[62:65], v[226:229], v[194:197], v[62:65] cbsz:4 blgp:4
	v_mfma_f32_16x16x128_f8f6f4 v[66:69], v[214:217], v[198:201], v[66:69] cbsz:4 blgp:4
	v_mfma_f32_16x16x128_f8f6f4 v[66:69], v[222:225], v[206:209], v[66:69] cbsz:4 blgp:4
	v_mfma_f32_16x16x128_f8f6f4 v[70:73], v[218:221], v[198:201], v[70:73] cbsz:4 blgp:4
	v_mfma_f32_16x16x128_f8f6f4 v[70:73], v[226:229], v[206:209], v[70:73] cbsz:4 blgp:4
	v_mfma_f32_16x16x128_f8f6f4 v[74:77], v[214:217], v[202:205], v[74:77] cbsz:4 blgp:4
	v_mfma_f32_16x16x128_f8f6f4 v[74:77], v[222:225], v[210:213], v[74:77] cbsz:4 blgp:4
	v_mfma_f32_16x16x128_f8f6f4 v[78:81], v[218:221], v[202:205], v[78:81] cbsz:4 blgp:4
	v_mfma_f32_16x16x128_f8f6f4 v[78:81], v[226:229], v[210:213], v[78:81] cbsz:4 blgp:4
	s_setprio 0
	s_barrier
	s_mov_b32 m0, s62
	s_nop 0
	global_load_lds_dwordx4 v164, s[36:37] sc1
	s_mov_b32 m0, s63
	s_nop 0
	global_load_lds_dwordx4 v168, s[36:37] sc1
	ds_read_b128 v[182:185], v179 offset:49152
	ds_read_b128 v[186:189], v179 offset:51200
	ds_read_b128 v[190:193], v180 offset:49152
	ds_read_b128 v[194:197], v180 offset:51200
	ds_read_b128 v[198:201], v179 offset:53248
	ds_read_b128 v[202:205], v179 offset:55296
	ds_read_b128 v[206:209], v180 offset:53248
	ds_read_b128 v[210:213], v180 offset:55296
	s_mov_b32 m0, s64
	s_nop 0
	global_load_lds_dwordx4 v162, s[40:41] sc1
	s_mov_b32 m0, s65
	s_nop 0
	global_load_lds_dwordx4 v166, s[40:41] sc1
	s_add_u32 s36, s36, s22
	s_addc_u32 s37, s37, s23
	s_mov_b32 m0, s66
	s_nop 0
	global_load_lds_dwordx4 v164, s[36:37] sc1
	s_mov_b32 m0, s67
	s_nop 0
	global_load_lds_dwordx4 v168, s[36:37] sc1
	s_waitcnt vmcnt(8)
	s_waitcnt lgkmcnt(0)
	s_barrier
	s_setprio 1
	v_mfma_f32_16x16x128_f8f6f4 v[86:89], v[146:149], v[182:185], v[86:89] cbsz:4 blgp:4
	v_mfma_f32_16x16x128_f8f6f4 v[86:89], v[154:157], v[190:193], v[86:89] cbsz:4 blgp:4
	v_mfma_f32_16x16x128_f8f6f4 v[90:93], v[150:153], v[182:185], v[90:93] cbsz:4 blgp:4
	v_mfma_f32_16x16x128_f8f6f4 v[90:93], v[158:161], v[190:193], v[90:93] cbsz:4 blgp:4
	v_mfma_f32_16x16x128_f8f6f4 v[98:101], v[146:149], v[186:189], v[98:101] cbsz:4 blgp:4
	v_mfma_f32_16x16x128_f8f6f4 v[98:101], v[154:157], v[194:197], v[98:101] cbsz:4 blgp:4
	v_mfma_f32_16x16x128_f8f6f4 v[106:109], v[150:153], v[186:189], v[106:109] cbsz:4 blgp:4
	v_mfma_f32_16x16x128_f8f6f4 v[106:109], v[158:161], v[194:197], v[106:109] cbsz:4 blgp:4
	v_mfma_f32_16x16x128_f8f6f4 v[118:121], v[146:149], v[198:201], v[118:121] cbsz:4 blgp:4
	v_mfma_f32_16x16x128_f8f6f4 v[118:121], v[154:157], v[206:209], v[118:121] cbsz:4 blgp:4
	v_mfma_f32_16x16x128_f8f6f4 v[126:129], v[150:153], v[198:201], v[126:129] cbsz:4 blgp:4
	v_mfma_f32_16x16x128_f8f6f4 v[126:129], v[158:161], v[206:209], v[126:129] cbsz:4 blgp:4
	v_mfma_f32_16x16x128_f8f6f4 v[138:141], v[146:149], v[202:205], v[138:141] cbsz:4 blgp:4
	v_mfma_f32_16x16x128_f8f6f4 v[138:141], v[154:157], v[210:213], v[138:141] cbsz:4 blgp:4
	v_mfma_f32_16x16x128_f8f6f4 v[82:85], v[150:153], v[202:205], v[82:85] cbsz:4 blgp:4
	v_mfma_f32_16x16x128_f8f6f4 v[82:85], v[158:161], v[210:213], v[82:85] cbsz:4 blgp:4
	v_mfma_f32_16x16x128_f8f6f4 v[94:97], v[214:217], v[182:185], v[94:97] cbsz:4 blgp:4
	v_mfma_f32_16x16x128_f8f6f4 v[94:97], v[222:225], v[190:193], v[94:97] cbsz:4 blgp:4
	v_mfma_f32_16x16x128_f8f6f4 v[102:105], v[218:221], v[182:185], v[102:105] cbsz:4 blgp:4
	v_mfma_f32_16x16x128_f8f6f4 v[102:105], v[226:229], v[190:193], v[102:105] cbsz:4 blgp:4
	v_mfma_f32_16x16x128_f8f6f4 v[110:113], v[214:217], v[186:189], v[110:113] cbsz:4 blgp:4
	v_mfma_f32_16x16x128_f8f6f4 v[110:113], v[222:225], v[194:197], v[110:113] cbsz:4 blgp:4
	v_mfma_f32_16x16x128_f8f6f4 v[114:117], v[218:221], v[186:189], v[114:117] cbsz:4 blgp:4
	v_mfma_f32_16x16x128_f8f6f4 v[114:117], v[226:229], v[194:197], v[114:117] cbsz:4 blgp:4
	v_mfma_f32_16x16x128_f8f6f4 v[122:125], v[214:217], v[198:201], v[122:125] cbsz:4 blgp:4
	v_mfma_f32_16x16x128_f8f6f4 v[122:125], v[222:225], v[206:209], v[122:125] cbsz:4 blgp:4
	v_mfma_f32_16x16x128_f8f6f4 v[130:133], v[218:221], v[198:201], v[130:133] cbsz:4 blgp:4
	v_mfma_f32_16x16x128_f8f6f4 v[130:133], v[226:229], v[206:209], v[130:133] cbsz:4 blgp:4
	v_mfma_f32_16x16x128_f8f6f4 v[134:137], v[214:217], v[202:205], v[134:137] cbsz:4 blgp:4
	v_mfma_f32_16x16x128_f8f6f4 v[134:137], v[222:225], v[210:213], v[134:137] cbsz:4 blgp:4
	v_mfma_f32_16x16x128_f8f6f4 v[142:145], v[218:221], v[202:205], v[142:145] cbsz:4 blgp:4
	v_mfma_f32_16x16x128_f8f6f4 v[142:145], v[226:229], v[210:213], v[142:145] cbsz:4 blgp:4
	s_setprio 0
	s_add_i32 s36, s82, 2
	s_add_u32 s31, s31, 0x100
	s_addc_u32 s46, s46, 0
	s_add_u32 s47, s47, 0x100
	s_addc_u32 s81, s81, 0
	s_add_u32 s34, s34, 0x100
	s_addc_u32 s35, s35, 0
	s_cmp_ge_i32 s82, s61
	s_barrier
	s_cbranch_scc1 .LBB6_20
	s_mov_b32 s82, s36
	s_cmp_eq_u32 s61, s82
	s_cselect_b64 s[36:37], -1, 0
	s_cmp_lg_u32 s61, s82
	s_cbranch_scc0 .LBB6_17
	s_branch .LBB6_18
